# MoE tail-fill conversion removed from phases 8/9: every layer converts all of its MoE weights (1536 items) inside its own attention phase
# baseline (speedup 1.0000x reference)
.LBB0_789:
	s_or_b64 exec, exec, s[2:3]
	v_readlane_b32 s2, v253, 55
	s_waitcnt lgkmcnt(0)
	s_barrier
	v_mov_b32_e32 v0, s2
	v_readlane_b32 s2, v253, 54
	ds_read_b32 v0, v0
	s_nop 0
	v_mov_b32_e32 v1, s2
	ds_read_b32 v1, v1
	s_waitcnt lgkmcnt(0)
	s_barrier
	v_add_u32_e32 v201, 0x580, v0
	s_nop 0
	v_readfirstlane_b32 s100, v201
	v_readlane_b32 s101, v254, 38
	s_nop 3
	s_movk_i32 vcc_lo, 0x600
	s_movk_i32 vcc_hi, 0xf00
	s_cmp_eq_u32 s101, 0
	s_cselect_b32 vcc_lo, 0x600, vcc_lo
	s_cselect_b32 vcc_hi, 0xf00, vcc_hi
	s_add_i32 vcc_lo, s100, vcc_lo
	s_max_u32 vcc_lo, vcc_lo, vcc_hi
	v_mov_b32_e32 v201, vcc_lo
	v_readfirstlane_b32 s30, v0
	v_cmp_ge_i32_e32 vcc, v1, v201
	v_readfirstlane_b32 s24, v1
	s_cbranch_vccnz .LBB0_931
	s_add_u32 s31, s4, 0x37b00000
	s_addc_u32 s34, s5, 0
	s_add_i32 s35, s30, 0x480
	s_add_u32 s44, s4, 0x61800000
	s_addc_u32 s45, s5, 0
	s_add_u32 s46, s4, 0x42c00000
	s_addc_u32 s47, s5, 0
	s_add_u32 s10, s4, 0x66d00000
	s_addc_u32 s11, s5, 0
	s_add_u32 s48, s4, 0x61640000
	s_movk_i32 s2, 0x100
	s_addc_u32 s49, s5, 0
	v_cmp_gt_i32_e64 s[38:39], s2, v199
	s_add_i32 s2, 0, 0x14800
	v_add_u32_e32 v214, s2, v200
	s_add_i32 s2, 0, 0x16800
	s_cmp_lg_u32 0, -1
	v_lshlrev_b32_e32 v3, 1, v199
	v_lshlrev_b32_e32 v211, 4, v199
	s_cselect_b32 s3, 0, 0
	v_lshlrev_b32_e32 v0, 3, v199
	v_lshlrev_b32_e32 v1, 10, v101
	v_lshlrev_b32_e32 v2, 4, v198
	v_and_b32_e32 v3, 32, v3
	v_and_b32_e32 v5, 0xc0, v211
	s_addk_i32 s3, 0x6000
	v_and_b32_e32 v210, 24, v0
	v_lshl_or_b32 v5, v101, 8, v5
	v_add3_u32 v213, 0, v1, v2
	v_add_u32_e32 v1, s3, v3
	v_add3_u32 v217, v1, v210, v5
	v_lshrrev_b32_e32 v1, 3, v100
	v_lshl_add_u32 v215, v198, 2, s2
	v_and_b32_e32 v218, 56, v0
	v_lshl_add_u32 v220, v1, 2, s2
	s_add_i32 s2, 0, 0x14a00
	v_add_u32_e32 v4, 0, v3
	v_lshlrev_b32_e32 v96, 1, v218
	v_add_u32_e32 v221, s2, v200
	s_add_i32 s2, 0, 0x14900
	v_ashrrev_i32_e32 v203, 31, v202
	v_lshlrev_b32_e32 v208, 9, v100
	v_lshrrev_b32_e32 v209, 2, v100
	v_add3_u32 v212, v4, v210, v5
	v_cmp_gt_u32_e64 s[40:41], 32, v100
	v_cmp_lt_u32_e64 s[42:43], 31, v100
	v_or_b32_e32 v216, 0xc0, v206
	v_lshl_add_u64 v[204:205], s[4:5], 0, v[96:97]
	v_lshlrev_b32_e32 v219, 7, v1
	v_add_u32_e32 v222, s2, v200
	v_lshlrev_b32_e32 v96, 1, v98
	s_branch .LBB0_792

.LBB0_796:
	s_or_b64 exec, exec, s[2:3]
	v_readlane_b32 s101, v254, 38
	s_nop 3
	s_branch .Lc3_l0
	s_cmpk_lt_u32 s24, 0xbe0
	s_cbranch_scc0 .Lc3_late

.Lc3_entry:
	v_readlane_b32 s22, v252, 0
	v_readlane_b32 s23, v252, 1
	v_readlane_b32 s20, v254, 38
	s_lshr_b32 s2, s93, 6
	s_load_dwordx2 s[24:25], s[22:23], 0x98
	s_lshl_b32 s27, s2, 14
	v_mbcnt_lo_u32_b32 v169, -1, 0
	v_mbcnt_hi_u32_b32 v169, -1, v169
	s_lshl_b32 s19, s101, 3
	s_add_i32 s19, s19, s2
	s_branch .Lc3_have

.LBB0_1474:
	s_cmp_lg_u32 s44, 3
	v_readlane_b32 s4, v253, 0
	s_cselect_b64 s[2:3], -1, 0
	v_readlane_b32 s5, v253, 1
	s_and_b64 s[2:3], s[2:3], s[4:5]
	s_andn2_b64 vcc, exec, s[2:3]
	s_branch .LBB0_1479
	s_ashr_i32 s2, s52, 6
	s_lshl_b32 s3, s2, 14
	s_add_i32 s4, s3, 0
	v_readlane_b32 s3, v253, 2
	s_add_i32 s6, s44, 1
	v_and_b32_e32 v6, 63, v198
	s_add_i32 s5, s3, s2
	s_mov_b64 s[2:3], -1
	s_cmpk_gt_i32 s5, 0x1fff
	v_lshlrev_b32_e32 v96, 2, v6
	s_cbranch_scc0 .LBB0_1477
	s_add_i32 s2, s5, 0xffffe000
	s_lshr_b32 s86, s2, 7
	s_load_dwordx2 s[2:3], s[8:9], 0x70
	s_lshl_b64 s[12:13], s[86:87], 20
	s_lshl_b32 s7, s6, 25
	s_add_u32 s12, s12, s7
	s_addc_u32 s13, s13, 0
	s_lshl_b64 s[14:15], s[12:13], 2
	s_waitcnt lgkmcnt(0)
	s_add_u32 s2, s2, s14
	s_addc_u32 s3, s3, s15
	s_add_u32 s10, s10, s12
	s_addc_u32 s11, s11, s13
	s_lshl_b32 s7, s5, 3
	s_and_b32 s12, s7, 0x380
	s_lshl_b32 s7, s5, 6
	s_and_b32 s7, s7, 0x3c0
	s_lshl_b32 s13, s12, 12
	s_add_u32 s2, s2, s13
	s_addc_u32 s3, s3, 0
	s_lshl_b32 s13, s7, 2
	s_add_u32 s2, s2, s13
	s_addc_u32 s3, s3, 0
	v_lshl_add_u64 v[0:1], s[2:3], 0, v[96:97]
	s_mov_b32 s13, 0x10000
	v_add_co_u32_e32 v2, vcc, s13, v0
	s_mov_b32 s13, 0xe000
	s_nop 0
	v_addc_co_u32_e32 v3, vcc, 0, v1, vcc
	v_add_co_u32_e32 v4, vcc, s13, v0
	s_mov_b32 s13, 0xd000
	s_nop 0
	v_addc_co_u32_e32 v5, vcc, 0, v1, vcc
	global_load_dword v7, v[2:3], off offset:-4096 nt
	global_load_dword v8, v[4:5], off nt
	v_add_co_u32_e32 v4, vcc, s13, v0
	s_mov_b32 s13, 0xc000
	s_nop 0
	v_addc_co_u32_e32 v5, vcc, 0, v1, vcc
	global_load_dword v9, v[4:5], off nt
	v_add_co_u32_e32 v4, vcc, s13, v0
	s_mov_b32 s13, 0xb000
	s_nop 0
	v_addc_co_u32_e32 v5, vcc, 0, v1, vcc
	global_load_dword v10, v[4:5], off nt
	v_add_co_u32_e32 v4, vcc, s13, v0
	s_mov_b32 s13, 0xa000
	s_nop 0
	v_addc_co_u32_e32 v5, vcc, 0, v1, vcc
	global_load_dword v11, v[4:5], off nt
	v_add_co_u32_e32 v4, vcc, s13, v0
	s_mov_b32 s13, 0x9000
	s_nop 0
	v_addc_co_u32_e32 v5, vcc, 0, v1, vcc
	global_load_dword v12, v[4:5], off nt
	v_add_co_u32_e32 v4, vcc, s13, v0
	s_mov_b32 s13, 0x8000
	s_nop 0
	v_addc_co_u32_e32 v5, vcc, 0, v1, vcc
	global_load_dword v13, v[4:5], off nt
	v_add_co_u32_e32 v4, vcc, s13, v0
	s_movk_i32 s13, 0x7000
	s_nop 0
	v_addc_co_u32_e32 v5, vcc, 0, v1, vcc
	global_load_dword v14, v[4:5], off nt
	v_add_co_u32_e32 v4, vcc, s13, v0
	s_movk_i32 s13, 0x6000
	s_nop 0
	v_addc_co_u32_e32 v5, vcc, 0, v1, vcc
	global_load_dword v15, v[4:5], off nt
	v_add_co_u32_e32 v4, vcc, s13, v0
	s_movk_i32 s13, 0x5000
	s_nop 0
	v_addc_co_u32_e32 v5, vcc, 0, v1, vcc
	global_load_dword v16, v[4:5], off nt
	v_add_co_u32_e32 v4, vcc, s13, v0
	s_movk_i32 s13, 0x4000
	s_nop 0
	v_addc_co_u32_e32 v5, vcc, 0, v1, vcc
	global_load_dword v17, v[4:5], off nt
	v_add_co_u32_e32 v4, vcc, s13, v0
	s_movk_i32 s13, 0x3000
	s_nop 0
	v_addc_co_u32_e32 v5, vcc, 0, v1, vcc
	global_load_dword v18, v[4:5], off nt
	v_add_co_u32_e32 v4, vcc, s13, v0
	s_movk_i32 s13, 0x2000
	s_nop 0
	v_addc_co_u32_e32 v5, vcc, 0, v1, vcc
	global_load_dword v19, v[4:5], off nt
	v_add_co_u32_e32 v4, vcc, s13, v0
	s_movk_i32 s13, 0x1000
	s_nop 0
	v_addc_co_u32_e32 v5, vcc, 0, v1, vcc
	global_load_dword v21, v[4:5], off nt
	v_add_co_u32_e32 v4, vcc, s13, v0
	s_nop 1
	v_addc_co_u32_e32 v5, vcc, 0, v1, vcc
	global_load_dword v23, v[4:5], off nt
	global_load_dword v26, v96, s[2:3] nt
	s_mov_b32 s2, 0x20000
	v_add_co_u32_e32 v4, vcc, s2, v0
	s_mov_b32 s2, 0x1e000
	s_nop 0
	v_addc_co_u32_e32 v5, vcc, 0, v1, vcc
	v_add_co_u32_e32 v24, vcc, s2, v0
	s_mov_b32 s2, 0x1d000
	s_nop 0
	v_addc_co_u32_e32 v25, vcc, 0, v1, vcc
	global_load_dword v20, v[4:5], off offset:-4096 nt
	global_load_dword v22, v[24:25], off nt
	v_add_co_u32_e32 v24, vcc, s2, v0
	s_mov_b32 s2, 0x1c000
	s_nop 0
	v_addc_co_u32_e32 v25, vcc, 0, v1, vcc
	v_add_co_u32_e32 v28, vcc, s2, v0
	s_mov_b32 s2, 0x1b000
	s_nop 0
	v_addc_co_u32_e32 v29, vcc, 0, v1, vcc
	global_load_dword v24, v[24:25], off nt
	s_nop 0
	global_load_dword v25, v[28:29], off nt
	v_add_co_u32_e32 v28, vcc, s2, v0
	s_mov_b32 s2, 0x1a000
	s_nop 0
	v_addc_co_u32_e32 v29, vcc, 0, v1, vcc
	global_load_dword v27, v[28:29], off nt
	v_add_co_u32_e32 v28, vcc, s2, v0
	s_mov_b32 s2, 0x19000
	s_nop 0
	v_addc_co_u32_e32 v29, vcc, 0, v1, vcc
	v_add_co_u32_e32 v30, vcc, s2, v0
	global_load_dword v28, v[28:29], off nt
	s_nop 0
	v_addc_co_u32_e32 v31, vcc, 0, v1, vcc
	global_load_dword v29, v[30:31], off nt
	v_add_co_u32_e32 v30, vcc, s94, v0
	s_mov_b32 s2, 0x17000
	s_nop 0
	v_addc_co_u32_e32 v31, vcc, 0, v1, vcc
	v_add_co_u32_e32 v32, vcc, s2, v0
	s_mov_b32 s2, 0x16000
	s_nop 0
	v_addc_co_u32_e32 v33, vcc, 0, v1, vcc
	global_load_dword v30, v[30:31], off nt
	s_nop 0
	global_load_dword v31, v[32:33], off nt
	v_add_co_u32_e32 v32, vcc, s2, v0
	s_mov_b32 s2, 0x15000
	s_nop 0
	v_addc_co_u32_e32 v33, vcc, 0, v1, vcc
	v_add_co_u32_e32 v34, vcc, s2, v0
	s_mov_b32 s2, 0x14000
	s_nop 0
	v_addc_co_u32_e32 v35, vcc, 0, v1, vcc
	global_load_dword v32, v[32:33], off nt
	s_nop 0
	global_load_dword v33, v[34:35], off nt
	v_add_co_u32_e32 v34, vcc, s2, v0
	s_mov_b32 s2, 0x13000
	s_nop 0
	v_addc_co_u32_e32 v35, vcc, 0, v1, vcc
	v_add_co_u32_e32 v36, vcc, s2, v0
	s_mov_b32 s2, 0x12000
	s_nop 0
	v_addc_co_u32_e32 v37, vcc, 0, v1, vcc
	v_add_co_u32_e32 v38, vcc, s2, v0
	s_mov_b32 s2, 0x11000
	s_nop 0
	v_addc_co_u32_e32 v39, vcc, 0, v1, vcc
	v_add_co_u32_e32 v40, vcc, s2, v0
	s_mov_b32 s2, 0x30000
	s_nop 0
	v_addc_co_u32_e32 v41, vcc, 0, v1, vcc
	global_load_dword v35, v[34:35], off nt
	s_nop 0
	global_load_dword v37, v[36:37], off nt
	s_nop 0
	global_load_dword v39, v[38:39], off nt
	s_nop 0
	global_load_dword v41, v[40:41], off nt
	s_nop 0
	global_load_dword v42, v[2:3], off nt
	v_add_co_u32_e32 v2, vcc, s2, v0
	s_mov_b32 s2, 0x2e000
	s_nop 0
	v_addc_co_u32_e32 v3, vcc, 0, v1, vcc
	v_add_co_u32_e32 v44, vcc, s2, v0
	s_mov_b32 s2, 0x2d000
	s_nop 0
	v_addc_co_u32_e32 v45, vcc, 0, v1, vcc
	global_load_dword v34, v[2:3], off offset:-4096 nt
	global_load_dword v36, v[44:45], off nt
	v_add_co_u32_e32 v44, vcc, s2, v0
	s_mov_b32 s2, 0x2c000
	s_nop 0
	v_addc_co_u32_e32 v45, vcc, 0, v1, vcc
	global_load_dword v38, v[44:45], off nt
	v_add_co_u32_e32 v44, vcc, s2, v0
	s_mov_b32 s2, 0x2b000
	s_nop 0
	v_addc_co_u32_e32 v45, vcc, 0, v1, vcc
	global_load_dword v40, v[44:45], off nt
	v_add_co_u32_e32 v44, vcc, s2, v0
	s_mov_b32 s2, 0x2a000
	s_nop 0
	v_addc_co_u32_e32 v45, vcc, 0, v1, vcc
	global_load_dword v43, v[44:45], off nt
	v_add_co_u32_e32 v44, vcc, s2, v0
	s_mov_b32 s2, 0x29000
	s_nop 0
	v_addc_co_u32_e32 v45, vcc, 0, v1, vcc
	v_add_co_u32_e32 v46, vcc, s2, v0
	s_mov_b32 s2, 0x28000
	s_nop 0
	v_addc_co_u32_e32 v47, vcc, 0, v1, vcc
	global_load_dword v44, v[44:45], off nt
	s_nop 0
	global_load_dword v45, v[46:47], off nt
	v_add_co_u32_e32 v46, vcc, s2, v0
	s_mov_b32 s2, 0x27000
	s_nop 0
	v_addc_co_u32_e32 v47, vcc, 0, v1, vcc
	v_add_co_u32_e32 v48, vcc, s2, v0
	s_mov_b32 s2, 0x26000
	s_nop 0
	v_addc_co_u32_e32 v49, vcc, 0, v1, vcc
	global_load_dword v46, v[46:47], off nt
	s_nop 0
	global_load_dword v47, v[48:49], off nt
	v_add_co_u32_e32 v48, vcc, s2, v0
	s_mov_b32 s2, 0x25000
	s_nop 0
	v_addc_co_u32_e32 v49, vcc, 0, v1, vcc
	v_add_co_u32_e32 v50, vcc, s2, v0
	s_mov_b32 s2, 0x24000
	s_nop 0
	v_addc_co_u32_e32 v51, vcc, 0, v1, vcc
	global_load_dword v48, v[48:49], off nt
	s_nop 0
	global_load_dword v49, v[50:51], off nt
	v_add_co_u32_e32 v50, vcc, s2, v0
	s_mov_b32 s2, 0x23000
	s_nop 0
	v_addc_co_u32_e32 v51, vcc, 0, v1, vcc
	v_add_co_u32_e32 v52, vcc, s2, v0
	s_mov_b32 s2, 0x22000
	s_nop 0
	v_addc_co_u32_e32 v53, vcc, 0, v1, vcc
	v_add_co_u32_e32 v54, vcc, s2, v0
	s_mov_b32 s2, 0x21000
	s_nop 0
	v_addc_co_u32_e32 v55, vcc, 0, v1, vcc
	v_add_co_u32_e32 v56, vcc, s2, v0
	s_mov_b32 s2, 0x40000
	s_nop 0
	v_addc_co_u32_e32 v57, vcc, 0, v1, vcc
	global_load_dword v51, v[50:51], off nt
	s_nop 0
	global_load_dword v53, v[52:53], off nt
	s_nop 0
	global_load_dword v55, v[54:55], off nt
	s_nop 0
	global_load_dword v57, v[56:57], off nt
	s_nop 0
	global_load_dword v58, v[4:5], off nt
	v_add_co_u32_e32 v4, vcc, s2, v0
	s_mov_b32 s2, 0x3e000
	s_nop 0
	v_addc_co_u32_e32 v5, vcc, 0, v1, vcc
	v_add_co_u32_e32 v60, vcc, s2, v0
	s_mov_b32 s2, 0x3d000
	s_nop 0
	v_addc_co_u32_e32 v61, vcc, 0, v1, vcc
	global_load_dword v50, v[4:5], off offset:-4096 nt
	global_load_dword v52, v[60:61], off nt
	v_add_co_u32_e32 v60, vcc, s2, v0
	s_mov_b32 s2, 0x3c000
	s_nop 0
	v_addc_co_u32_e32 v61, vcc, 0, v1, vcc
	global_load_dword v54, v[60:61], off nt
	v_add_co_u32_e32 v60, vcc, s2, v0
	s_mov_b32 s2, 0x3b000
	s_nop 0
	v_addc_co_u32_e32 v61, vcc, 0, v1, vcc
	global_load_dword v56, v[60:61], off nt
	v_add_co_u32_e32 v60, vcc, s2, v0
	s_mov_b32 s2, 0x3a000
	s_nop 0
	v_addc_co_u32_e32 v61, vcc, 0, v1, vcc
	global_load_dword v59, v[60:61], off nt
	v_add_co_u32_e32 v60, vcc, s2, v0
	s_mov_b32 s2, 0x39000
	s_nop 0
	v_addc_co_u32_e32 v61, vcc, 0, v1, vcc
	v_add_co_u32_e32 v62, vcc, s2, v0
	s_mov_b32 s2, 0x38000
	s_nop 0
	v_addc_co_u32_e32 v63, vcc, 0, v1, vcc
	global_load_dword v60, v[60:61], off nt
	s_nop 0
	global_load_dword v61, v[62:63], off nt
	v_add_co_u32_e32 v62, vcc, s2, v0
	s_mov_b32 s2, 0x37000
	s_nop 0
	v_addc_co_u32_e32 v63, vcc, 0, v1, vcc
	v_add_co_u32_e32 v64, vcc, s2, v0
	s_mov_b32 s2, 0x36000
	s_nop 0
	v_addc_co_u32_e32 v65, vcc, 0, v1, vcc
	global_load_dword v62, v[62:63], off nt
	s_nop 0
	global_load_dword v63, v[64:65], off nt
	v_add_co_u32_e32 v64, vcc, s2, v0
	s_mov_b32 s2, 0x35000
	s_nop 0
	v_addc_co_u32_e32 v65, vcc, 0, v1, vcc
	v_add_co_u32_e32 v66, vcc, s2, v0
	s_mov_b32 s2, 0x34000
	s_nop 0
	v_addc_co_u32_e32 v67, vcc, 0, v1, vcc
	global_load_dword v64, v[64:65], off nt
	s_nop 0
	global_load_dword v65, v[66:67], off nt
	v_add_co_u32_e32 v66, vcc, s2, v0
	s_mov_b32 s2, 0x33000
	s_nop 0
	v_addc_co_u32_e32 v67, vcc, 0, v1, vcc
	v_add_co_u32_e32 v68, vcc, s2, v0
	s_mov_b32 s2, 0x32000
	s_nop 0
	v_addc_co_u32_e32 v69, vcc, 0, v1, vcc
	v_add_co_u32_e32 v70, vcc, s2, v0
	s_mov_b32 s2, 0x31000
	s_nop 0
	v_addc_co_u32_e32 v71, vcc, 0, v1, vcc
	v_add_co_u32_e32 v72, vcc, s2, v0
	s_mov_b32 s2, 0x50000
	s_nop 0
	v_addc_co_u32_e32 v73, vcc, 0, v1, vcc
	global_load_dword v67, v[66:67], off nt
	s_nop 0
	global_load_dword v69, v[68:69], off nt
	s_nop 0
	global_load_dword v71, v[70:71], off nt
	s_nop 0
	global_load_dword v73, v[72:73], off nt
	s_nop 0
	global_load_dword v74, v[2:3], off nt
	v_add_co_u32_e32 v2, vcc, s2, v0
	s_mov_b32 s2, 0x4e000
	s_nop 0
	v_addc_co_u32_e32 v3, vcc, 0, v1, vcc
	v_add_co_u32_e32 v76, vcc, s2, v0
	s_mov_b32 s2, 0x4d000
	s_nop 0
	v_addc_co_u32_e32 v77, vcc, 0, v1, vcc
	global_load_dword v66, v[2:3], off offset:-4096 nt
	global_load_dword v68, v[76:77], off nt
	v_add_co_u32_e32 v76, vcc, s2, v0
	s_mov_b32 s2, 0x4c000
	s_nop 0
	v_addc_co_u32_e32 v77, vcc, 0, v1, vcc
	global_load_dword v70, v[76:77], off nt
	v_add_co_u32_e32 v76, vcc, s2, v0
	s_mov_b32 s2, 0x4b000
	s_nop 0
	v_addc_co_u32_e32 v77, vcc, 0, v1, vcc
	global_load_dword v72, v[76:77], off nt
	v_add_co_u32_e32 v76, vcc, s2, v0
	s_mov_b32 s2, 0x4a000
	s_nop 0
	v_addc_co_u32_e32 v77, vcc, 0, v1, vcc
	global_load_dword v75, v[76:77], off nt
	v_add_co_u32_e32 v76, vcc, s2, v0
	s_mov_b32 s2, 0x49000
	s_nop 0
	v_addc_co_u32_e32 v77, vcc, 0, v1, vcc
	v_add_co_u32_e32 v78, vcc, s2, v0
	s_mov_b32 s2, 0x48000
	s_nop 0
	v_addc_co_u32_e32 v79, vcc, 0, v1, vcc
	global_load_dword v76, v[76:77], off nt
	s_nop 0
	global_load_dword v77, v[78:79], off nt
	v_add_co_u32_e32 v78, vcc, s2, v0
	s_mov_b32 s2, 0x47000
	s_nop 0
	v_addc_co_u32_e32 v79, vcc, 0, v1, vcc
	v_add_co_u32_e32 v80, vcc, s2, v0
	s_mov_b32 s2, 0x46000
	s_nop 0
	v_addc_co_u32_e32 v81, vcc, 0, v1, vcc
	global_load_dword v78, v[78:79], off nt
	s_nop 0
	global_load_dword v79, v[80:81], off nt
	v_add_co_u32_e32 v80, vcc, s2, v0
	s_mov_b32 s2, 0x45000
	s_nop 0
	v_addc_co_u32_e32 v81, vcc, 0, v1, vcc
	v_add_co_u32_e32 v82, vcc, s2, v0
	s_mov_b32 s2, 0x44000
	s_nop 0
	v_addc_co_u32_e32 v83, vcc, 0, v1, vcc
	global_load_dword v80, v[80:81], off nt
	s_nop 0
	global_load_dword v81, v[82:83], off nt
	v_add_co_u32_e32 v82, vcc, s2, v0
	s_mov_b32 s2, 0x43000
	s_nop 0
	v_addc_co_u32_e32 v83, vcc, 0, v1, vcc
	v_add_co_u32_e32 v84, vcc, s2, v0
	s_mov_b32 s2, 0x42000
	s_nop 0
	v_addc_co_u32_e32 v85, vcc, 0, v1, vcc
	v_add_co_u32_e32 v86, vcc, s2, v0
	s_mov_b32 s2, 0x41000
	s_nop 0
	v_addc_co_u32_e32 v87, vcc, 0, v1, vcc
	v_add_co_u32_e32 v88, vcc, s2, v0
	s_mov_b32 s2, 0x60000
	s_nop 0
	v_addc_co_u32_e32 v89, vcc, 0, v1, vcc
	global_load_dword v83, v[82:83], off nt
	s_nop 0
	global_load_dword v85, v[84:85], off nt
	s_nop 0
	global_load_dword v87, v[86:87], off nt
	s_nop 0
	global_load_dword v89, v[88:89], off nt
	s_nop 0
	global_load_dword v90, v[4:5], off nt
	v_add_co_u32_e32 v4, vcc, s2, v0
	s_mov_b32 s2, 0x5e000
	s_nop 0
	v_addc_co_u32_e32 v5, vcc, 0, v1, vcc
	v_add_co_u32_e32 v92, vcc, s2, v0
	s_mov_b32 s2, 0x5d000
	s_nop 0
	v_addc_co_u32_e32 v93, vcc, 0, v1, vcc
	global_load_dword v82, v[4:5], off offset:-4096 nt
	global_load_dword v84, v[92:93], off nt
	v_add_co_u32_e32 v92, vcc, s2, v0
	s_mov_b32 s2, 0x5c000
	s_nop 0
	v_addc_co_u32_e32 v93, vcc, 0, v1, vcc
	global_load_dword v86, v[92:93], off nt
	v_add_co_u32_e32 v92, vcc, s2, v0
	s_mov_b32 s2, 0x5b000
	s_nop 0
	v_addc_co_u32_e32 v93, vcc, 0, v1, vcc
	global_load_dword v88, v[92:93], off nt
	v_add_co_u32_e32 v92, vcc, s2, v0
	s_mov_b32 s2, 0x5a000
	s_nop 0
	v_addc_co_u32_e32 v93, vcc, 0, v1, vcc
	global_load_dword v91, v[92:93], off nt
	v_add_co_u32_e32 v92, vcc, s2, v0
	s_mov_b32 s2, 0x59000
	s_nop 0
	v_addc_co_u32_e32 v93, vcc, 0, v1, vcc
	v_add_co_u32_e32 v94, vcc, s2, v0
	s_mov_b32 s2, 0x58000
	s_nop 0
	v_addc_co_u32_e32 v95, vcc, 0, v1, vcc
	global_load_dword v92, v[92:93], off nt
	s_nop 0
	global_load_dword v93, v[94:95], off nt
	v_add_co_u32_e32 v94, vcc, s2, v0
	s_mov_b32 s2, 0x57000
	s_nop 0
	v_addc_co_u32_e32 v95, vcc, 0, v1, vcc
	v_add_co_u32_e32 v98, vcc, s2, v0
	s_mov_b32 s2, 0x56000
	s_nop 0
	v_addc_co_u32_e32 v99, vcc, 0, v1, vcc
	global_load_dword v94, v[94:95], off nt
	s_nop 0
	global_load_dword v95, v[98:99], off nt
	v_add_co_u32_e32 v98, vcc, s2, v0
	s_mov_b32 s2, 0x55000
	s_nop 0
	v_addc_co_u32_e32 v99, vcc, 0, v1, vcc
	v_add_co_u32_e32 v100, vcc, s2, v0
	s_mov_b32 s2, 0x54000
	s_nop 0
	v_addc_co_u32_e32 v101, vcc, 0, v1, vcc
	global_load_dword v98, v[98:99], off nt
	s_nop 0
	global_load_dword v99, v[100:101], off nt
	v_add_co_u32_e32 v100, vcc, s2, v0
	s_mov_b32 s2, 0x53000
	s_nop 0
	v_addc_co_u32_e32 v101, vcc, 0, v1, vcc
	v_add_co_u32_e32 v102, vcc, s2, v0
	s_mov_b32 s2, 0x52000
	s_nop 0
	v_addc_co_u32_e32 v103, vcc, 0, v1, vcc
	global_load_dword v101, v[100:101], off nt
	s_nop 0
	global_load_dword v104, v[102:103], off nt
	v_add_co_u32_e32 v102, vcc, s2, v0
	s_mov_b32 s2, 0x51000
	s_nop 0
	v_addc_co_u32_e32 v103, vcc, 0, v1, vcc
	global_load_dword v105, v[102:103], off nt
	v_add_co_u32_e32 v102, vcc, s2, v0
	s_mov_b32 s2, 0x70000
	s_nop 0
	v_addc_co_u32_e32 v103, vcc, 0, v1, vcc
	global_load_dword v106, v[102:103], off nt
	global_load_dword v107, v[2:3], off nt
	v_add_co_u32_e32 v2, vcc, s2, v0
	s_mov_b32 s2, 0x6e000
	s_nop 0
	v_addc_co_u32_e32 v3, vcc, 0, v1, vcc
	v_add_co_u32_e32 v102, vcc, s2, v0
	s_mov_b32 s2, 0x6d000
	s_nop 0
	v_addc_co_u32_e32 v103, vcc, 0, v1, vcc
	global_load_dword v100, v[2:3], off offset:-4096 nt
	global_load_dword v108, v[102:103], off nt
	v_add_co_u32_e32 v102, vcc, s2, v0
	s_mov_b32 s2, 0x6c000
	s_nop 0
	v_addc_co_u32_e32 v103, vcc, 0, v1, vcc
	global_load_dword v109, v[102:103], off nt
	v_add_co_u32_e32 v102, vcc, s2, v0
	s_mov_b32 s2, 0x6b000
	s_nop 0
	v_addc_co_u32_e32 v103, vcc, 0, v1, vcc
	global_load_dword v110, v[102:103], off nt
	v_add_co_u32_e32 v102, vcc, s2, v0
	s_mov_b32 s2, 0x6a000
	s_nop 0
	v_addc_co_u32_e32 v103, vcc, 0, v1, vcc
	global_load_dword v111, v[102:103], off nt
	v_add_co_u32_e32 v102, vcc, s2, v0
	s_mov_b32 s2, 0x69000
	s_nop 0
	v_addc_co_u32_e32 v103, vcc, 0, v1, vcc
	global_load_dword v112, v[102:103], off nt
	v_add_co_u32_e32 v102, vcc, s2, v0
	s_mov_b32 s2, 0x68000
	s_nop 0
	v_addc_co_u32_e32 v103, vcc, 0, v1, vcc
	global_load_dword v113, v[102:103], off nt
	v_add_co_u32_e32 v102, vcc, s2, v0
	s_mov_b32 s2, 0x67000
	s_nop 0
	v_addc_co_u32_e32 v103, vcc, 0, v1, vcc
	global_load_dword v114, v[102:103], off nt
	v_add_co_u32_e32 v102, vcc, s2, v0
	s_mov_b32 s2, 0x66000
	s_nop 0
	v_addc_co_u32_e32 v103, vcc, 0, v1, vcc
	global_load_dword v115, v[102:103], off nt
	v_add_co_u32_e32 v102, vcc, s2, v0
	s_mov_b32 s2, 0x65000
	s_nop 0
	v_addc_co_u32_e32 v103, vcc, 0, v1, vcc
	global_load_dword v116, v[102:103], off nt
	v_add_co_u32_e32 v102, vcc, s2, v0
	s_mov_b32 s2, 0x64000
	s_nop 0
	v_addc_co_u32_e32 v103, vcc, 0, v1, vcc
	global_load_dword v117, v[102:103], off nt
	v_add_co_u32_e32 v102, vcc, s2, v0
	s_mov_b32 s2, 0x63000
	s_nop 0
	v_addc_co_u32_e32 v103, vcc, 0, v1, vcc
	global_load_dword v118, v[102:103], off nt
	v_add_co_u32_e32 v102, vcc, s2, v0
	s_mov_b32 s2, 0x62000
	s_nop 0
	v_addc_co_u32_e32 v103, vcc, 0, v1, vcc
	global_load_dword v119, v[102:103], off nt
	v_add_co_u32_e32 v102, vcc, s2, v0
	s_mov_b32 s2, 0x61000
	s_nop 0
	v_addc_co_u32_e32 v103, vcc, 0, v1, vcc
	global_load_dword v120, v[102:103], off nt
	v_add_co_u32_e32 v102, vcc, s2, v0
	s_mov_b32 s2, 0x7f000
	s_nop 0
	v_addc_co_u32_e32 v103, vcc, 0, v1, vcc
	global_load_dword v102, v[102:103], off nt
	s_nop 0
	global_load_dword v103, v[4:5], off nt
	v_add_co_u32_e32 v4, vcc, s2, v0
	s_mov_b32 s2, 0x7e000
	s_nop 0
	v_addc_co_u32_e32 v5, vcc, 0, v1, vcc
	global_load_dword v121, v[4:5], off nt
	v_add_co_u32_e32 v4, vcc, s2, v0
	s_mov_b32 s2, 0x7d000
	s_nop 0
	v_addc_co_u32_e32 v5, vcc, 0, v1, vcc
	global_load_dword v122, v[4:5], off nt
	v_add_co_u32_e32 v4, vcc, s2, v0
	s_mov_b32 s2, 0x7c000
	s_nop 0
	v_addc_co_u32_e32 v5, vcc, 0, v1, vcc
	global_load_dword v123, v[4:5], off nt
	v_add_co_u32_e32 v4, vcc, s2, v0
	s_mov_b32 s2, 0x7b000
	s_nop 0
	v_addc_co_u32_e32 v5, vcc, 0, v1, vcc
	global_load_dword v124, v[4:5], off nt
	v_add_co_u32_e32 v4, vcc, s2, v0
	s_mov_b32 s2, 0x7a000
	s_nop 0
	v_addc_co_u32_e32 v5, vcc, 0, v1, vcc
	global_load_dword v125, v[4:5], off nt
	v_add_co_u32_e32 v4, vcc, s2, v0
	s_mov_b32 s2, 0x79000
	s_nop 0
	v_addc_co_u32_e32 v5, vcc, 0, v1, vcc
	global_load_dword v126, v[4:5], off nt
	v_add_co_u32_e32 v4, vcc, s2, v0
	s_mov_b32 s2, 0x78000
	s_nop 0
	v_addc_co_u32_e32 v5, vcc, 0, v1, vcc
	global_load_dword v127, v[4:5], off nt
	v_add_co_u32_e32 v4, vcc, s2, v0
	s_mov_b32 s2, 0x77000
	s_nop 0
	v_addc_co_u32_e32 v5, vcc, 0, v1, vcc
	global_load_dword v128, v[4:5], off nt
	v_add_co_u32_e32 v4, vcc, s2, v0
	s_mov_b32 s2, 0x76000
	s_nop 0
	v_addc_co_u32_e32 v5, vcc, 0, v1, vcc
	global_load_dword v129, v[4:5], off nt
	v_add_co_u32_e32 v4, vcc, s2, v0
	s_mov_b32 s2, 0x75000
	s_nop 0
	v_addc_co_u32_e32 v5, vcc, 0, v1, vcc
	global_load_dword v130, v[4:5], off nt
	v_add_co_u32_e32 v4, vcc, s2, v0
	s_mov_b32 s2, 0x74000
	s_nop 0
	v_addc_co_u32_e32 v5, vcc, 0, v1, vcc
	global_load_dword v131, v[4:5], off nt
	v_add_co_u32_e32 v4, vcc, s2, v0
	s_mov_b32 s2, 0x73000
	s_nop 0
	v_addc_co_u32_e32 v5, vcc, 0, v1, vcc
	global_load_dword v132, v[4:5], off nt
	v_add_co_u32_e32 v4, vcc, s2, v0
	s_mov_b32 s2, 0x72000
	s_nop 0
	v_addc_co_u32_e32 v5, vcc, 0, v1, vcc
	global_load_dword v133, v[4:5], off nt
	v_add_co_u32_e32 v4, vcc, s2, v0
	s_mov_b32 s2, 0x71000
	s_nop 0
	v_addc_co_u32_e32 v5, vcc, 0, v1, vcc
	v_add_co_u32_e32 v0, vcc, s2, v0
	global_load_dword v4, v[4:5], off nt
	s_nop 0
	v_addc_co_u32_e32 v1, vcc, 0, v1, vcc
	global_load_dword v5, v[0:1], off nt
	global_load_dword v134, v[2:3], off nt
	v_mov_b32_e32 v0, s4
	s_movk_i32 s2, 0x90
	s_waitcnt vmcnt(62)
	v_mad_u32_u24 v135, v6, s2, v0
	v_mul_f32_e32 v1, 0x42800000, v26
	v_mul_f32_e32 v2, 0x42800000, v23
	v_mov_b32_e32 v0, v97
	v_cvt_pk_fp8_f32 v0, v1, v2
	v_mul_f32_e32 v3, 0x42800000, v21
	v_mul_f32_e32 v19, 0x42800000, v19
	v_mul_f32_e32 v2, 0x42800000, v18
	v_cvt_pk_fp8_f32 v0, v3, v19 op_sel:[0,0,1]
	v_mul_f32_e32 v3, 0x42800000, v17
	v_mov_b32_e32 v1, v97
	v_cvt_pk_fp8_f32 v1, v2, v3
	v_mul_f32_e32 v3, 0x42800000, v14
	v_mul_f32_e32 v13, 0x42800000, v13
	v_mov_b32_e32 v2, v97
	v_cvt_pk_fp8_f32 v2, v3, v13
	v_mul_f32_e32 v10, 0x42800000, v10
	v_mul_f32_e32 v9, 0x42800000, v9
	v_mov_b32_e32 v3, v97
	v_cvt_pk_fp8_f32 v3, v10, v9
	v_mul_f32_e32 v16, 0x42800000, v16
	v_mul_f32_e32 v15, 0x42800000, v15
	v_mul_f32_e32 v12, 0x42800000, v12
	v_mul_f32_e32 v11, 0x42800000, v11
	v_mul_f32_e32 v8, 0x42800000, v8
	v_mul_f32_e32 v7, 0x42800000, v7
	v_cvt_pk_fp8_f32 v1, v16, v15 op_sel:[0,0,1]
	v_cvt_pk_fp8_f32 v2, v12, v11 op_sel:[0,0,1]
	v_cvt_pk_fp8_f32 v3, v8, v7 op_sel:[0,0,1]
	s_waitcnt vmcnt(48)
	s_waitcnt vmcnt(32)
	s_waitcnt vmcnt(16)
	s_waitcnt vmcnt(0)
	ds_write_b128 v135, v[0:3]
	v_mul_f32_e32 v1, 0x42800000, v42
	v_mul_f32_e32 v2, 0x42800000, v41
	v_mov_b32_e32 v0, v97
	v_cvt_pk_fp8_f32 v0, v1, v2
	v_mul_f32_e32 v3, 0x42800000, v39
	v_mul_f32_e32 v7, 0x42800000, v37
	v_mul_f32_e32 v2, 0x42800000, v35
	v_cvt_pk_fp8_f32 v0, v3, v7 op_sel:[0,0,1]
	v_mul_f32_e32 v3, 0x42800000, v33
	v_mov_b32_e32 v1, v97
	v_cvt_pk_fp8_f32 v1, v2, v3
	v_mul_f32_e32 v7, 0x42800000, v32
	v_mul_f32_e32 v8, 0x42800000, v31
	v_mul_f32_e32 v3, 0x42800000, v30
	v_cvt_pk_fp8_f32 v1, v7, v8 op_sel:[0,0,1]
	v_mul_f32_e32 v7, 0x42800000, v29
	v_mov_b32_e32 v2, v97
	v_cvt_pk_fp8_f32 v2, v3, v7
	v_mul_f32_e32 v8, 0x42800000, v28
	v_mul_f32_e32 v9, 0x42800000, v27
	v_mul_f32_e32 v7, 0x42800000, v25
	v_cvt_pk_fp8_f32 v2, v8, v9 op_sel:[0,0,1]
	v_mul_f32_e32 v8, 0x42800000, v24
	v_mov_b32_e32 v3, v97
	v_cvt_pk_fp8_f32 v3, v7, v8
	v_mul_f32_e32 v9, 0x42800000, v22
	v_mul_f32_e32 v10, 0x42800000, v20
	v_mul_f32_e32 v7, 0x42800000, v53
	v_cvt_pk_fp8_f32 v3, v9, v10 op_sel:[0,0,1]
	v_mul_f32_e32 v8, 0x42800000, v47
	v_mul_f32_e32 v9, 0x42800000, v43
	v_mul_f32_e32 v10, 0x42800000, v34
	ds_write_b128 v135, v[0:3] offset:16
	v_mul_f32_e32 v1, 0x42800000, v58
	v_mul_f32_e32 v2, 0x42800000, v57
	v_mov_b32_e32 v0, v97
	v_cvt_pk_fp8_f32 v0, v1, v2
	v_mul_f32_e32 v3, 0x42800000, v55
	v_mul_f32_e32 v2, 0x42800000, v51
	v_mov_b32_e32 v1, v97
	v_cvt_pk_fp8_f32 v0, v3, v7 op_sel:[0,0,1]
	v_mul_f32_e32 v3, 0x42800000, v49
	v_cvt_pk_fp8_f32 v1, v2, v3
	v_mul_f32_e32 v7, 0x42800000, v48
	v_mul_f32_e32 v3, 0x42800000, v46
	v_mov_b32_e32 v2, v97
	v_cvt_pk_fp8_f32 v1, v7, v8 op_sel:[0,0,1]
	v_mul_f32_e32 v7, 0x42800000, v45
	v_cvt_pk_fp8_f32 v2, v3, v7
	v_mul_f32_e32 v8, 0x42800000, v44
	v_mul_f32_e32 v7, 0x42800000, v40
	v_mov_b32_e32 v3, v97
	v_cvt_pk_fp8_f32 v2, v8, v9 op_sel:[0,0,1]
	v_mul_f32_e32 v8, 0x42800000, v38
	v_cvt_pk_fp8_f32 v3, v7, v8
	v_mul_f32_e32 v9, 0x42800000, v36
	v_mul_f32_e32 v7, 0x42800000, v69
	v_mul_f32_e32 v8, 0x42800000, v63
	v_cvt_pk_fp8_f32 v3, v9, v10 op_sel:[0,0,1]
	v_mul_f32_e32 v9, 0x42800000, v59
	v_mul_f32_e32 v10, 0x42800000, v50
	s_add_u32 s2, s10, s12
	ds_write_b128 v135, v[0:3] offset:32
	v_mul_f32_e32 v1, 0x42800000, v74
	v_mul_f32_e32 v2, 0x42800000, v73
	v_mov_b32_e32 v0, v97
	v_cvt_pk_fp8_f32 v0, v1, v2
	v_mul_f32_e32 v3, 0x42800000, v71
	v_mul_f32_e32 v2, 0x42800000, v67
	v_mov_b32_e32 v1, v97
	v_cvt_pk_fp8_f32 v0, v3, v7 op_sel:[0,0,1]
	v_mul_f32_e32 v3, 0x42800000, v65
	v_cvt_pk_fp8_f32 v1, v2, v3
	v_mul_f32_e32 v7, 0x42800000, v64
	v_mul_f32_e32 v3, 0x42800000, v62
	v_mov_b32_e32 v2, v97
	v_cvt_pk_fp8_f32 v1, v7, v8 op_sel:[0,0,1]
	v_mul_f32_e32 v7, 0x42800000, v61
	v_cvt_pk_fp8_f32 v2, v3, v7
	v_mul_f32_e32 v8, 0x42800000, v60
	v_mul_f32_e32 v7, 0x42800000, v56
	v_mov_b32_e32 v3, v97
	v_cvt_pk_fp8_f32 v2, v8, v9 op_sel:[0,0,1]
	v_mul_f32_e32 v8, 0x42800000, v54
	v_cvt_pk_fp8_f32 v3, v7, v8
	v_mul_f32_e32 v9, 0x42800000, v52
	v_mul_f32_e32 v7, 0x42800000, v85
	v_mul_f32_e32 v8, 0x42800000, v79
	v_cvt_pk_fp8_f32 v3, v9, v10 op_sel:[0,0,1]
	v_mul_f32_e32 v9, 0x42800000, v75
	v_mul_f32_e32 v10, 0x42800000, v66
	s_addc_u32 s3, s11, 0
	ds_write_b128 v135, v[0:3] offset:48
	v_mul_f32_e32 v1, 0x42800000, v90
	v_mul_f32_e32 v2, 0x42800000, v89
	v_mov_b32_e32 v0, v97
	v_cvt_pk_fp8_f32 v0, v1, v2
	v_mul_f32_e32 v3, 0x42800000, v87
	v_mul_f32_e32 v2, 0x42800000, v83
	v_mov_b32_e32 v1, v97
	v_cvt_pk_fp8_f32 v0, v3, v7 op_sel:[0,0,1]
	v_mul_f32_e32 v3, 0x42800000, v81
	v_cvt_pk_fp8_f32 v1, v2, v3
	v_mul_f32_e32 v7, 0x42800000, v80
	v_mul_f32_e32 v3, 0x42800000, v78
	v_mov_b32_e32 v2, v97
	v_cvt_pk_fp8_f32 v1, v7, v8 op_sel:[0,0,1]
	v_mul_f32_e32 v7, 0x42800000, v77
	v_cvt_pk_fp8_f32 v2, v3, v7
	v_mul_f32_e32 v8, 0x42800000, v76
	v_mul_f32_e32 v7, 0x42800000, v72
	v_mov_b32_e32 v3, v97
	v_cvt_pk_fp8_f32 v2, v8, v9 op_sel:[0,0,1]
	v_mul_f32_e32 v8, 0x42800000, v70
	v_cvt_pk_fp8_f32 v3, v7, v8
	v_mul_f32_e32 v9, 0x42800000, v68
	v_mul_f32_e32 v7, 0x42800000, v104
	v_mul_f32_e32 v8, 0x42800000, v95
	v_cvt_pk_fp8_f32 v3, v9, v10 op_sel:[0,0,1]
	v_mul_f32_e32 v9, 0x42800000, v91
	v_mul_f32_e32 v10, 0x42800000, v82
	ds_write_b128 v135, v[0:3] offset:64
	v_mul_f32_e32 v1, 0x42800000, v107
	v_mul_f32_e32 v2, 0x42800000, v106
	v_mov_b32_e32 v0, v97
	v_cvt_pk_fp8_f32 v0, v1, v2
	v_mul_f32_e32 v3, 0x42800000, v105
	v_mul_f32_e32 v2, 0x42800000, v101
	v_mov_b32_e32 v1, v97
	v_cvt_pk_fp8_f32 v0, v3, v7 op_sel:[0,0,1]
	v_mul_f32_e32 v3, 0x42800000, v99
	v_cvt_pk_fp8_f32 v1, v2, v3
	v_mul_f32_e32 v7, 0x42800000, v98
	v_mul_f32_e32 v3, 0x42800000, v94
	v_mov_b32_e32 v2, v97
	v_cvt_pk_fp8_f32 v1, v7, v8 op_sel:[0,0,1]
	v_mul_f32_e32 v7, 0x42800000, v93
	v_cvt_pk_fp8_f32 v2, v3, v7
	v_mul_f32_e32 v8, 0x42800000, v92
	v_mul_f32_e32 v7, 0x42800000, v88
	v_mov_b32_e32 v3, v97
	v_cvt_pk_fp8_f32 v2, v8, v9 op_sel:[0,0,1]
	v_mul_f32_e32 v8, 0x42800000, v86
	v_cvt_pk_fp8_f32 v3, v7, v8
	v_mul_f32_e32 v9, 0x42800000, v84
	v_mul_f32_e32 v7, 0x42800000, v119
	v_mul_f32_e32 v8, 0x42800000, v115
	v_cvt_pk_fp8_f32 v3, v9, v10 op_sel:[0,0,1]
	v_mul_f32_e32 v9, 0x42800000, v111
	v_mul_f32_e32 v10, 0x42800000, v100
	ds_write_b128 v135, v[0:3] offset:80
	v_mul_f32_e32 v1, 0x42800000, v103
	v_mul_f32_e32 v2, 0x42800000, v102
	v_mov_b32_e32 v0, v97
	v_cvt_pk_fp8_f32 v0, v1, v2
	v_mul_f32_e32 v3, 0x42800000, v120
	v_mul_f32_e32 v2, 0x42800000, v118
	v_mov_b32_e32 v1, v97
	v_cvt_pk_fp8_f32 v0, v3, v7 op_sel:[0,0,1]
	v_mul_f32_e32 v3, 0x42800000, v117
	v_cvt_pk_fp8_f32 v1, v2, v3
	v_mul_f32_e32 v7, 0x42800000, v116
	v_mul_f32_e32 v3, 0x42800000, v114
	v_mov_b32_e32 v2, v97
	v_cvt_pk_fp8_f32 v1, v7, v8 op_sel:[0,0,1]
	v_mul_f32_e32 v7, 0x42800000, v113
	v_cvt_pk_fp8_f32 v2, v3, v7
	v_mul_f32_e32 v8, 0x42800000, v112
	v_mul_f32_e32 v7, 0x42800000, v110
	v_mov_b32_e32 v3, v97
	v_cvt_pk_fp8_f32 v2, v8, v9 op_sel:[0,0,1]
	v_mul_f32_e32 v8, 0x42800000, v109
	v_cvt_pk_fp8_f32 v3, v7, v8
	v_mul_f32_e32 v9, 0x42800000, v108
	v_mul_f32_e32 v7, 0x42800000, v125
	v_mul_f32_e32 v8, 0x42800000, v121
	v_cvt_pk_fp8_f32 v3, v9, v10 op_sel:[0,0,1]
	v_mov_b32_e32 v9, v97
	ds_write_b128 v135, v[0:3] offset:96
	v_mul_f32_e32 v1, 0x42800000, v134
	v_mul_f32_e32 v2, 0x42800000, v5
	v_mov_b32_e32 v0, v97
	v_cvt_pk_fp8_f32 v0, v1, v2
	v_mul_f32_e32 v3, 0x42800000, v4
	v_mul_f32_e32 v4, 0x42800000, v133
	v_mul_f32_e32 v2, 0x42800000, v132
	v_cvt_pk_fp8_f32 v0, v3, v4 op_sel:[0,0,1]
	v_mul_f32_e32 v3, 0x42800000, v131
	v_mov_b32_e32 v1, v97
	v_cvt_pk_fp8_f32 v1, v2, v3
	v_mul_f32_e32 v4, 0x42800000, v130
	v_mul_f32_e32 v5, 0x42800000, v129
	v_mul_f32_e32 v3, 0x42800000, v128
	v_cvt_pk_fp8_f32 v1, v4, v5 op_sel:[0,0,1]
	v_mul_f32_e32 v4, 0x42800000, v127
	v_mov_b32_e32 v2, v97
	v_cvt_pk_fp8_f32 v2, v3, v4
	v_mul_f32_e32 v5, 0x42800000, v126
	v_mul_f32_e32 v4, 0x42800000, v124
	v_mov_b32_e32 v3, v97
	v_cvt_pk_fp8_f32 v2, v5, v7 op_sel:[0,0,1]
	v_mul_f32_e32 v5, 0x42800000, v123
	v_cvt_pk_fp8_f32 v3, v4, v5
	v_mul_f32_e32 v7, 0x42800000, v122
	v_cvt_pk_fp8_f32 v3, v7, v8 op_sel:[0,0,1]
	v_lshrrev_b32_e32 v8, 3, v6
	ds_write_b128 v135, v[0:3] offset:112
	v_lshlrev_b32_e32 v0, 4, v6
	v_and_b32_e32 v0, 0x70, v0
	v_mov_b32_e32 v1, v97
	v_lshl_add_u64 v[2:3], s[2:3], 0, v[0:1]
	v_mul_u32_u24_e32 v1, 0x90, v8
	s_waitcnt lgkmcnt(0)
	s_mov_b64 s[2:3], 0x23b00000
	v_add3_u32 v7, s4, v0, v1
	v_lshl_add_u64 v[4:5], v[2:3], 0, s[2:3]
	ds_read_b128 v[0:3], v7
	v_or_b32_e32 v8, s7, v8
	v_lshlrev_b32_e32 v8, 10, v8
	v_lshl_add_u64 v[10:11], v[4:5], 0, v[8:9]
	s_mov_b64 s[2:3], 0
	s_waitcnt lgkmcnt(0)
	global_store_dwordx4 v[10:11], v[0:3], off
	ds_read_b128 v[0:3], v7 offset:1152
	v_or_b32_e32 v10, 0x2000, v8
	v_mov_b32_e32 v11, v97
	v_lshl_add_u64 v[10:11], v[4:5], 0, v[10:11]
	s_waitcnt lgkmcnt(0)
	global_store_dwordx4 v[10:11], v[0:3], off
	ds_read_b128 v[0:3], v7 offset:2304
	v_or_b32_e32 v10, 0x4000, v8
	v_mov_b32_e32 v11, v97
	v_lshl_add_u64 v[10:11], v[4:5], 0, v[10:11]
	s_waitcnt lgkmcnt(0)
	global_store_dwordx4 v[10:11], v[0:3], off
	ds_read_b128 v[0:3], v7 offset:3456
	v_or_b32_e32 v10, 0x6000, v8
	v_mov_b32_e32 v11, v97
	v_lshl_add_u64 v[10:11], v[4:5], 0, v[10:11]
	s_waitcnt lgkmcnt(0)
	global_store_dwordx4 v[10:11], v[0:3], off
	ds_read_b128 v[0:3], v7 offset:4608
	v_or_b32_e32 v10, 0x8000, v8
	v_mov_b32_e32 v11, v97
	v_lshl_add_u64 v[10:11], v[4:5], 0, v[10:11]
	s_waitcnt lgkmcnt(0)
	global_store_dwordx4 v[10:11], v[0:3], off
	ds_read_b128 v[0:3], v7 offset:5760
	v_or_b32_e32 v10, 0xa000, v8
	v_mov_b32_e32 v11, v97
	v_lshl_add_u64 v[10:11], v[4:5], 0, v[10:11]
	s_waitcnt lgkmcnt(0)
	global_store_dwordx4 v[10:11], v[0:3], off
	ds_read_b128 v[0:3], v7 offset:6912
	v_or_b32_e32 v10, 0xc000, v8
	v_mov_b32_e32 v11, v97
	v_lshl_add_u64 v[10:11], v[4:5], 0, v[10:11]
	v_or_b32_e32 v8, 0xe000, v8
	s_waitcnt lgkmcnt(0)
	global_store_dwordx4 v[10:11], v[0:3], off
	ds_read_b128 v[0:3], v7 offset:8064
	v_lshl_add_u64 v[4:5], v[4:5], 0, v[8:9]
	s_waitcnt lgkmcnt(0)
	global_store_dwordx4 v[4:5], v[0:3], off
	s_waitcnt lgkmcnt(0)

.LBB0_1582:
	s_cmp_lg_u32 s44, 3
	v_readlane_b32 s4, v253, 9
	s_cselect_b64 s[2:3], -1, 0
	v_readlane_b32 s5, v253, 10
	s_and_b64 s[2:3], s[2:3], s[4:5]
	s_andn2_b64 vcc, exec, s[2:3]
	s_branch .LBB0_1587
	s_ashr_i32 s2, s52, 6
	s_lshl_b32 s3, s2, 14
	s_add_i32 s4, s3, 0
	v_readlane_b32 s3, v253, 11
	s_add_i32 s6, s44, 1
	v_and_b32_e32 v6, 63, v130
	s_add_i32 s5, s3, s2
	s_mov_b64 s[2:3], -1
	s_cmpk_gt_i32 s5, 0x1fff
	v_lshlrev_b32_e32 v96, 2, v6
	s_cbranch_scc0 .LBB0_1585
	s_add_i32 s2, s5, 0xffffe000
	s_lshr_b32 s86, s2, 7
	s_load_dwordx2 s[2:3], s[10:11], 0x70
	s_lshl_b64 s[12:13], s[86:87], 20
	s_lshl_b32 s7, s6, 25
	s_add_u32 s12, s12, s7
	s_addc_u32 s13, s13, 0
	s_lshl_b64 s[14:15], s[12:13], 2
	s_waitcnt lgkmcnt(0)
	s_add_u32 s2, s2, s14
	s_addc_u32 s3, s3, s15
	s_add_u32 s12, s53, s12
	s_addc_u32 s13, s54, s13
	s_lshl_b32 s7, s5, 3
	s_and_b32 s14, s7, 0x380
	s_lshl_b32 s7, s5, 6
	s_and_b32 s7, s7, 0x3c0
	s_lshl_b32 s15, s14, 12
	s_add_u32 s2, s2, s15
	s_addc_u32 s3, s3, 0
	s_lshl_b32 s15, s7, 2
	s_add_u32 s2, s2, s15
	s_addc_u32 s3, s3, 0
	v_lshl_add_u64 v[0:1], s[2:3], 0, v[96:97]
	s_mov_b32 s15, 0x10000
	v_add_co_u32_e32 v2, vcc, s15, v0
	s_mov_b32 s15, 0xe000
	s_nop 0
	v_addc_co_u32_e32 v3, vcc, 0, v1, vcc
	v_add_co_u32_e32 v4, vcc, s15, v0
	s_mov_b32 s15, 0xd000
	s_nop 0
	v_addc_co_u32_e32 v5, vcc, 0, v1, vcc
	global_load_dword v7, v[2:3], off offset:-4096 nt
	global_load_dword v8, v[4:5], off nt
	v_add_co_u32_e32 v4, vcc, s15, v0
	s_mov_b32 s15, 0xc000
	s_nop 0
	v_addc_co_u32_e32 v5, vcc, 0, v1, vcc
	global_load_dword v9, v[4:5], off nt
	v_add_co_u32_e32 v4, vcc, s15, v0
	s_mov_b32 s15, 0xb000
	s_nop 0
	v_addc_co_u32_e32 v5, vcc, 0, v1, vcc
	global_load_dword v10, v[4:5], off nt
	v_add_co_u32_e32 v4, vcc, s15, v0
	s_mov_b32 s15, 0xa000
	s_nop 0
	v_addc_co_u32_e32 v5, vcc, 0, v1, vcc
	global_load_dword v11, v[4:5], off nt
	v_add_co_u32_e32 v4, vcc, s15, v0
	s_mov_b32 s15, 0x9000
	s_nop 0
	v_addc_co_u32_e32 v5, vcc, 0, v1, vcc
	global_load_dword v12, v[4:5], off nt
	v_add_co_u32_e32 v4, vcc, s15, v0
	s_mov_b32 s15, 0x8000
	s_nop 0
	v_addc_co_u32_e32 v5, vcc, 0, v1, vcc
	global_load_dword v13, v[4:5], off nt
	v_add_co_u32_e32 v4, vcc, s15, v0
	s_movk_i32 s15, 0x7000
	s_nop 0
	v_addc_co_u32_e32 v5, vcc, 0, v1, vcc
	global_load_dword v14, v[4:5], off nt
	v_add_co_u32_e32 v4, vcc, s15, v0
	s_movk_i32 s15, 0x6000
	s_nop 0
	v_addc_co_u32_e32 v5, vcc, 0, v1, vcc
	global_load_dword v15, v[4:5], off nt
	v_add_co_u32_e32 v4, vcc, s15, v0
	s_movk_i32 s15, 0x5000
	s_nop 0
	v_addc_co_u32_e32 v5, vcc, 0, v1, vcc
	global_load_dword v16, v[4:5], off nt
	v_add_co_u32_e32 v4, vcc, s15, v0
	s_movk_i32 s15, 0x4000
	s_nop 0
	v_addc_co_u32_e32 v5, vcc, 0, v1, vcc
	global_load_dword v17, v[4:5], off nt
	v_add_co_u32_e32 v4, vcc, s15, v0
	s_movk_i32 s15, 0x3000
	s_nop 0
	v_addc_co_u32_e32 v5, vcc, 0, v1, vcc
	global_load_dword v18, v[4:5], off nt
	v_add_co_u32_e32 v4, vcc, s15, v0
	s_movk_i32 s15, 0x2000
	s_nop 0
	v_addc_co_u32_e32 v5, vcc, 0, v1, vcc
	global_load_dword v19, v[4:5], off nt
	v_add_co_u32_e32 v4, vcc, s15, v0
	s_movk_i32 s15, 0x1000
	s_nop 0
	v_addc_co_u32_e32 v5, vcc, 0, v1, vcc
	global_load_dword v21, v[4:5], off nt
	v_add_co_u32_e32 v4, vcc, s15, v0
	s_nop 1
	v_addc_co_u32_e32 v5, vcc, 0, v1, vcc
	global_load_dword v23, v[4:5], off nt
	global_load_dword v26, v96, s[2:3] nt
	s_mov_b32 s2, 0x20000
	v_add_co_u32_e32 v4, vcc, s2, v0
	s_mov_b32 s2, 0x1e000
	s_nop 0
	v_addc_co_u32_e32 v5, vcc, 0, v1, vcc
	v_add_co_u32_e32 v24, vcc, s2, v0
	s_mov_b32 s2, 0x1d000
	s_nop 0
	v_addc_co_u32_e32 v25, vcc, 0, v1, vcc
	global_load_dword v20, v[4:5], off offset:-4096 nt
	global_load_dword v22, v[24:25], off nt
	v_add_co_u32_e32 v24, vcc, s2, v0
	s_mov_b32 s2, 0x1c000
	s_nop 0
	v_addc_co_u32_e32 v25, vcc, 0, v1, vcc
	v_add_co_u32_e32 v28, vcc, s2, v0
	s_mov_b32 s2, 0x1b000
	s_nop 0
	v_addc_co_u32_e32 v29, vcc, 0, v1, vcc
	global_load_dword v24, v[24:25], off nt
	s_nop 0
	global_load_dword v25, v[28:29], off nt
	v_add_co_u32_e32 v28, vcc, s2, v0
	s_mov_b32 s2, 0x1a000
	s_nop 0
	v_addc_co_u32_e32 v29, vcc, 0, v1, vcc
	global_load_dword v27, v[28:29], off nt
	v_add_co_u32_e32 v28, vcc, s2, v0
	s_mov_b32 s2, 0x19000
	s_nop 0
	v_addc_co_u32_e32 v29, vcc, 0, v1, vcc
	v_add_co_u32_e32 v30, vcc, s2, v0
	global_load_dword v28, v[28:29], off nt
	s_nop 0
	v_addc_co_u32_e32 v31, vcc, 0, v1, vcc
	global_load_dword v29, v[30:31], off nt
	v_add_co_u32_e32 v30, vcc, s94, v0
	s_mov_b32 s2, 0x17000
	s_nop 0
	v_addc_co_u32_e32 v31, vcc, 0, v1, vcc
	v_add_co_u32_e32 v32, vcc, s2, v0
	s_mov_b32 s2, 0x16000
	s_nop 0
	v_addc_co_u32_e32 v33, vcc, 0, v1, vcc
	global_load_dword v30, v[30:31], off nt
	s_nop 0
	global_load_dword v31, v[32:33], off nt
	v_add_co_u32_e32 v32, vcc, s2, v0
	s_mov_b32 s2, 0x15000
	s_nop 0
	v_addc_co_u32_e32 v33, vcc, 0, v1, vcc
	v_add_co_u32_e32 v34, vcc, s2, v0
	s_mov_b32 s2, 0x14000
	s_nop 0
	v_addc_co_u32_e32 v35, vcc, 0, v1, vcc
	global_load_dword v32, v[32:33], off nt
	s_nop 0
	global_load_dword v33, v[34:35], off nt
	v_add_co_u32_e32 v34, vcc, s2, v0
	s_mov_b32 s2, 0x13000
	s_nop 0
	v_addc_co_u32_e32 v35, vcc, 0, v1, vcc
	v_add_co_u32_e32 v36, vcc, s2, v0
	s_mov_b32 s2, 0x12000
	s_nop 0
	v_addc_co_u32_e32 v37, vcc, 0, v1, vcc
	v_add_co_u32_e32 v38, vcc, s2, v0
	s_mov_b32 s2, 0x11000
	s_nop 0
	v_addc_co_u32_e32 v39, vcc, 0, v1, vcc
	v_add_co_u32_e32 v40, vcc, s2, v0
	s_mov_b32 s2, 0x30000
	s_nop 0
	v_addc_co_u32_e32 v41, vcc, 0, v1, vcc
	global_load_dword v35, v[34:35], off nt
	s_nop 0
	global_load_dword v37, v[36:37], off nt
	s_nop 0
	global_load_dword v39, v[38:39], off nt
	s_nop 0
	global_load_dword v41, v[40:41], off nt
	s_nop 0
	global_load_dword v42, v[2:3], off nt
	v_add_co_u32_e32 v2, vcc, s2, v0
	s_mov_b32 s2, 0x2e000
	s_nop 0
	v_addc_co_u32_e32 v3, vcc, 0, v1, vcc
	v_add_co_u32_e32 v44, vcc, s2, v0
	s_mov_b32 s2, 0x2d000
	s_nop 0
	v_addc_co_u32_e32 v45, vcc, 0, v1, vcc
	global_load_dword v34, v[2:3], off offset:-4096 nt
	global_load_dword v36, v[44:45], off nt
	v_add_co_u32_e32 v44, vcc, s2, v0
	s_mov_b32 s2, 0x2c000
	s_nop 0
	v_addc_co_u32_e32 v45, vcc, 0, v1, vcc
	global_load_dword v38, v[44:45], off nt
	v_add_co_u32_e32 v44, vcc, s2, v0
	s_mov_b32 s2, 0x2b000
	s_nop 0
	v_addc_co_u32_e32 v45, vcc, 0, v1, vcc
	global_load_dword v40, v[44:45], off nt
	v_add_co_u32_e32 v44, vcc, s2, v0
	s_mov_b32 s2, 0x2a000
	s_nop 0
	v_addc_co_u32_e32 v45, vcc, 0, v1, vcc
	global_load_dword v43, v[44:45], off nt
	v_add_co_u32_e32 v44, vcc, s2, v0
	s_mov_b32 s2, 0x29000
	s_nop 0
	v_addc_co_u32_e32 v45, vcc, 0, v1, vcc
	v_add_co_u32_e32 v46, vcc, s2, v0
	s_mov_b32 s2, 0x28000
	s_nop 0
	v_addc_co_u32_e32 v47, vcc, 0, v1, vcc
	global_load_dword v44, v[44:45], off nt
	s_nop 0
	global_load_dword v45, v[46:47], off nt
	v_add_co_u32_e32 v46, vcc, s2, v0
	s_mov_b32 s2, 0x27000
	s_nop 0
	v_addc_co_u32_e32 v47, vcc, 0, v1, vcc
	v_add_co_u32_e32 v48, vcc, s2, v0
	s_mov_b32 s2, 0x26000
	s_nop 0
	v_addc_co_u32_e32 v49, vcc, 0, v1, vcc
	global_load_dword v46, v[46:47], off nt
	s_nop 0
	global_load_dword v47, v[48:49], off nt
	v_add_co_u32_e32 v48, vcc, s2, v0
	s_mov_b32 s2, 0x25000
	s_nop 0
	v_addc_co_u32_e32 v49, vcc, 0, v1, vcc
	v_add_co_u32_e32 v50, vcc, s2, v0
	s_mov_b32 s2, 0x24000
	s_nop 0
	v_addc_co_u32_e32 v51, vcc, 0, v1, vcc
	global_load_dword v48, v[48:49], off nt
	s_nop 0
	global_load_dword v49, v[50:51], off nt
	v_add_co_u32_e32 v50, vcc, s2, v0
	s_mov_b32 s2, 0x23000
	s_nop 0
	v_addc_co_u32_e32 v51, vcc, 0, v1, vcc
	v_add_co_u32_e32 v52, vcc, s2, v0
	s_mov_b32 s2, 0x22000
	s_nop 0
	v_addc_co_u32_e32 v53, vcc, 0, v1, vcc
	v_add_co_u32_e32 v54, vcc, s2, v0
	s_mov_b32 s2, 0x21000
	s_nop 0
	v_addc_co_u32_e32 v55, vcc, 0, v1, vcc
	v_add_co_u32_e32 v56, vcc, s2, v0
	s_mov_b32 s2, 0x40000
	s_nop 0
	v_addc_co_u32_e32 v57, vcc, 0, v1, vcc
	global_load_dword v51, v[50:51], off nt
	s_nop 0
	global_load_dword v53, v[52:53], off nt
	s_nop 0
	global_load_dword v55, v[54:55], off nt
	s_nop 0
	global_load_dword v57, v[56:57], off nt
	s_nop 0
	global_load_dword v58, v[4:5], off nt
	v_add_co_u32_e32 v4, vcc, s2, v0
	s_mov_b32 s2, 0x3e000
	s_nop 0
	v_addc_co_u32_e32 v5, vcc, 0, v1, vcc
	v_add_co_u32_e32 v60, vcc, s2, v0
	s_mov_b32 s2, 0x3d000
	s_nop 0
	v_addc_co_u32_e32 v61, vcc, 0, v1, vcc
	global_load_dword v50, v[4:5], off offset:-4096 nt
	global_load_dword v52, v[60:61], off nt
	v_add_co_u32_e32 v60, vcc, s2, v0
	s_mov_b32 s2, 0x3c000
	s_nop 0
	v_addc_co_u32_e32 v61, vcc, 0, v1, vcc
	global_load_dword v54, v[60:61], off nt
	v_add_co_u32_e32 v60, vcc, s2, v0
	s_mov_b32 s2, 0x3b000
	s_nop 0
	v_addc_co_u32_e32 v61, vcc, 0, v1, vcc
	global_load_dword v56, v[60:61], off nt
	v_add_co_u32_e32 v60, vcc, s2, v0
	s_mov_b32 s2, 0x3a000
	s_nop 0
	v_addc_co_u32_e32 v61, vcc, 0, v1, vcc
	global_load_dword v59, v[60:61], off nt
	v_add_co_u32_e32 v60, vcc, s2, v0
	s_mov_b32 s2, 0x39000
	s_nop 0
	v_addc_co_u32_e32 v61, vcc, 0, v1, vcc
	v_add_co_u32_e32 v62, vcc, s2, v0
	s_mov_b32 s2, 0x38000
	s_nop 0
	v_addc_co_u32_e32 v63, vcc, 0, v1, vcc
	global_load_dword v60, v[60:61], off nt
	s_nop 0
	global_load_dword v61, v[62:63], off nt
	v_add_co_u32_e32 v62, vcc, s2, v0
	s_mov_b32 s2, 0x37000
	s_nop 0
	v_addc_co_u32_e32 v63, vcc, 0, v1, vcc
	v_add_co_u32_e32 v64, vcc, s2, v0
	s_mov_b32 s2, 0x36000
	s_nop 0
	v_addc_co_u32_e32 v65, vcc, 0, v1, vcc
	global_load_dword v62, v[62:63], off nt
	s_nop 0
	global_load_dword v63, v[64:65], off nt
	v_add_co_u32_e32 v64, vcc, s2, v0
	s_mov_b32 s2, 0x35000
	s_nop 0
	v_addc_co_u32_e32 v65, vcc, 0, v1, vcc
	v_add_co_u32_e32 v66, vcc, s2, v0
	s_mov_b32 s2, 0x34000
	s_nop 0
	v_addc_co_u32_e32 v67, vcc, 0, v1, vcc
	global_load_dword v64, v[64:65], off nt
	s_nop 0
	global_load_dword v65, v[66:67], off nt
	v_add_co_u32_e32 v66, vcc, s2, v0
	s_mov_b32 s2, 0x33000
	s_nop 0
	v_addc_co_u32_e32 v67, vcc, 0, v1, vcc
	v_add_co_u32_e32 v68, vcc, s2, v0
	s_mov_b32 s2, 0x32000
	s_nop 0
	v_addc_co_u32_e32 v69, vcc, 0, v1, vcc
	v_add_co_u32_e32 v70, vcc, s2, v0
	s_mov_b32 s2, 0x31000
	s_nop 0
	v_addc_co_u32_e32 v71, vcc, 0, v1, vcc
	v_add_co_u32_e32 v72, vcc, s2, v0
	s_mov_b32 s2, 0x50000
	s_nop 0
	v_addc_co_u32_e32 v73, vcc, 0, v1, vcc
	global_load_dword v67, v[66:67], off nt
	s_nop 0
	global_load_dword v69, v[68:69], off nt
	s_nop 0
	global_load_dword v71, v[70:71], off nt
	s_nop 0
	global_load_dword v73, v[72:73], off nt
	s_nop 0
	global_load_dword v74, v[2:3], off nt
	v_add_co_u32_e32 v2, vcc, s2, v0
	s_mov_b32 s2, 0x4e000
	s_nop 0
	v_addc_co_u32_e32 v3, vcc, 0, v1, vcc
	v_add_co_u32_e32 v76, vcc, s2, v0
	s_mov_b32 s2, 0x4d000
	s_nop 0
	v_addc_co_u32_e32 v77, vcc, 0, v1, vcc
	global_load_dword v66, v[2:3], off offset:-4096 nt
	global_load_dword v68, v[76:77], off nt
	v_add_co_u32_e32 v76, vcc, s2, v0
	s_mov_b32 s2, 0x4c000
	s_nop 0
	v_addc_co_u32_e32 v77, vcc, 0, v1, vcc
	global_load_dword v70, v[76:77], off nt
	v_add_co_u32_e32 v76, vcc, s2, v0
	s_mov_b32 s2, 0x4b000
	s_nop 0
	v_addc_co_u32_e32 v77, vcc, 0, v1, vcc
	global_load_dword v72, v[76:77], off nt
	v_add_co_u32_e32 v76, vcc, s2, v0
	s_mov_b32 s2, 0x4a000
	s_nop 0
	v_addc_co_u32_e32 v77, vcc, 0, v1, vcc
	global_load_dword v75, v[76:77], off nt
	v_add_co_u32_e32 v76, vcc, s2, v0
	s_mov_b32 s2, 0x49000
	s_nop 0
	v_addc_co_u32_e32 v77, vcc, 0, v1, vcc
	v_add_co_u32_e32 v78, vcc, s2, v0
	s_mov_b32 s2, 0x48000
	s_nop 0
	v_addc_co_u32_e32 v79, vcc, 0, v1, vcc
	global_load_dword v76, v[76:77], off nt
	s_nop 0
	global_load_dword v77, v[78:79], off nt
	v_add_co_u32_e32 v78, vcc, s2, v0
	s_mov_b32 s2, 0x47000
	s_nop 0
	v_addc_co_u32_e32 v79, vcc, 0, v1, vcc
	v_add_co_u32_e32 v80, vcc, s2, v0
	s_mov_b32 s2, 0x46000
	s_nop 0
	v_addc_co_u32_e32 v81, vcc, 0, v1, vcc
	global_load_dword v78, v[78:79], off nt
	s_nop 0
	global_load_dword v79, v[80:81], off nt
	v_add_co_u32_e32 v80, vcc, s2, v0
	s_mov_b32 s2, 0x45000
	s_nop 0
	v_addc_co_u32_e32 v81, vcc, 0, v1, vcc
	v_add_co_u32_e32 v82, vcc, s2, v0
	s_mov_b32 s2, 0x44000
	s_nop 0
	v_addc_co_u32_e32 v83, vcc, 0, v1, vcc
	global_load_dword v80, v[80:81], off nt
	s_nop 0
	global_load_dword v81, v[82:83], off nt
	v_add_co_u32_e32 v82, vcc, s2, v0
	s_mov_b32 s2, 0x43000
	s_nop 0
	v_addc_co_u32_e32 v83, vcc, 0, v1, vcc
	v_add_co_u32_e32 v84, vcc, s2, v0
	s_mov_b32 s2, 0x42000
	s_nop 0
	v_addc_co_u32_e32 v85, vcc, 0, v1, vcc
	v_add_co_u32_e32 v86, vcc, s2, v0
	s_mov_b32 s2, 0x41000
	s_nop 0
	v_addc_co_u32_e32 v87, vcc, 0, v1, vcc
	v_add_co_u32_e32 v88, vcc, s2, v0
	s_mov_b32 s2, 0x60000
	s_nop 0
	v_addc_co_u32_e32 v89, vcc, 0, v1, vcc
	global_load_dword v83, v[82:83], off nt
	s_nop 0
	global_load_dword v85, v[84:85], off nt
	s_nop 0
	global_load_dword v87, v[86:87], off nt
	s_nop 0
	global_load_dword v89, v[88:89], off nt
	s_nop 0
	global_load_dword v90, v[4:5], off nt
	v_add_co_u32_e32 v4, vcc, s2, v0
	s_mov_b32 s2, 0x5e000
	s_nop 0
	v_addc_co_u32_e32 v5, vcc, 0, v1, vcc
	v_add_co_u32_e32 v92, vcc, s2, v0
	s_mov_b32 s2, 0x5d000
	s_nop 0
	v_addc_co_u32_e32 v93, vcc, 0, v1, vcc
	global_load_dword v82, v[4:5], off offset:-4096 nt
	global_load_dword v84, v[92:93], off nt
	v_add_co_u32_e32 v92, vcc, s2, v0
	s_mov_b32 s2, 0x5c000
	s_nop 0
	v_addc_co_u32_e32 v93, vcc, 0, v1, vcc
	global_load_dword v86, v[92:93], off nt
	v_add_co_u32_e32 v92, vcc, s2, v0
	s_mov_b32 s2, 0x5b000
	s_nop 0
	v_addc_co_u32_e32 v93, vcc, 0, v1, vcc
	global_load_dword v88, v[92:93], off nt
	v_add_co_u32_e32 v92, vcc, s2, v0
	s_mov_b32 s2, 0x5a000
	s_nop 0
	v_addc_co_u32_e32 v93, vcc, 0, v1, vcc
	global_load_dword v91, v[92:93], off nt
	v_add_co_u32_e32 v92, vcc, s2, v0
	s_mov_b32 s2, 0x59000
	s_nop 0
	v_addc_co_u32_e32 v93, vcc, 0, v1, vcc
	v_add_co_u32_e32 v94, vcc, s2, v0
	s_mov_b32 s2, 0x58000
	s_nop 0
	v_addc_co_u32_e32 v95, vcc, 0, v1, vcc
	global_load_dword v92, v[92:93], off nt
	s_nop 0
	global_load_dword v93, v[94:95], off nt
	v_add_co_u32_e32 v94, vcc, s2, v0
	s_mov_b32 s2, 0x57000
	s_nop 0
	v_addc_co_u32_e32 v95, vcc, 0, v1, vcc
	v_add_co_u32_e32 v98, vcc, s2, v0
	s_mov_b32 s2, 0x56000
	s_nop 0
	v_addc_co_u32_e32 v99, vcc, 0, v1, vcc
	global_load_dword v94, v[94:95], off nt
	s_nop 0
	global_load_dword v95, v[98:99], off nt
	v_add_co_u32_e32 v98, vcc, s2, v0
	s_mov_b32 s2, 0x55000
	s_nop 0
	v_addc_co_u32_e32 v99, vcc, 0, v1, vcc
	v_add_co_u32_e32 v100, vcc, s2, v0
	s_mov_b32 s2, 0x54000
	s_nop 0
	v_addc_co_u32_e32 v101, vcc, 0, v1, vcc
	global_load_dword v98, v[98:99], off nt
	s_nop 0
	global_load_dword v99, v[100:101], off nt
	v_add_co_u32_e32 v100, vcc, s2, v0
	s_mov_b32 s2, 0x53000
	s_nop 0
	v_addc_co_u32_e32 v101, vcc, 0, v1, vcc
	v_add_co_u32_e32 v102, vcc, s2, v0
	s_mov_b32 s2, 0x52000
	s_nop 0
	v_addc_co_u32_e32 v103, vcc, 0, v1, vcc
	global_load_dword v101, v[100:101], off nt
	s_nop 0
	global_load_dword v104, v[102:103], off nt
	v_add_co_u32_e32 v102, vcc, s2, v0
	s_mov_b32 s2, 0x51000
	s_nop 0
	v_addc_co_u32_e32 v103, vcc, 0, v1, vcc
	global_load_dword v105, v[102:103], off nt
	v_add_co_u32_e32 v102, vcc, s2, v0
	s_mov_b32 s2, 0x70000
	s_nop 0
	v_addc_co_u32_e32 v103, vcc, 0, v1, vcc
	global_load_dword v106, v[102:103], off nt
	global_load_dword v107, v[2:3], off nt
	v_add_co_u32_e32 v2, vcc, s2, v0
	s_mov_b32 s2, 0x6e000
	s_nop 0
	v_addc_co_u32_e32 v3, vcc, 0, v1, vcc
	v_add_co_u32_e32 v102, vcc, s2, v0
	s_mov_b32 s2, 0x6d000
	s_nop 0
	v_addc_co_u32_e32 v103, vcc, 0, v1, vcc
	global_load_dword v100, v[2:3], off offset:-4096 nt
	global_load_dword v108, v[102:103], off nt
	v_add_co_u32_e32 v102, vcc, s2, v0
	s_mov_b32 s2, 0x6c000
	s_nop 0
	v_addc_co_u32_e32 v103, vcc, 0, v1, vcc
	global_load_dword v109, v[102:103], off nt
	v_add_co_u32_e32 v102, vcc, s2, v0
	s_mov_b32 s2, 0x6b000
	s_nop 0
	v_addc_co_u32_e32 v103, vcc, 0, v1, vcc
	global_load_dword v110, v[102:103], off nt
	v_add_co_u32_e32 v102, vcc, s2, v0
	s_mov_b32 s2, 0x6a000
	s_nop 0
	v_addc_co_u32_e32 v103, vcc, 0, v1, vcc
	global_load_dword v111, v[102:103], off nt
	v_add_co_u32_e32 v102, vcc, s2, v0
	s_mov_b32 s2, 0x69000
	s_nop 0
	v_addc_co_u32_e32 v103, vcc, 0, v1, vcc
	global_load_dword v112, v[102:103], off nt
	v_add_co_u32_e32 v102, vcc, s2, v0
	s_mov_b32 s2, 0x68000
	s_nop 0
	v_addc_co_u32_e32 v103, vcc, 0, v1, vcc
	global_load_dword v113, v[102:103], off nt
	v_add_co_u32_e32 v102, vcc, s2, v0
	s_mov_b32 s2, 0x67000
	s_nop 0
	v_addc_co_u32_e32 v103, vcc, 0, v1, vcc
	global_load_dword v114, v[102:103], off nt
	v_add_co_u32_e32 v102, vcc, s2, v0
	s_mov_b32 s2, 0x66000
	s_nop 0
	v_addc_co_u32_e32 v103, vcc, 0, v1, vcc
	global_load_dword v115, v[102:103], off nt
	v_add_co_u32_e32 v102, vcc, s2, v0
	s_mov_b32 s2, 0x65000
	s_nop 0
	v_addc_co_u32_e32 v103, vcc, 0, v1, vcc
	global_load_dword v116, v[102:103], off nt
	v_add_co_u32_e32 v102, vcc, s2, v0
	s_mov_b32 s2, 0x64000
	s_nop 0
	v_addc_co_u32_e32 v103, vcc, 0, v1, vcc
	global_load_dword v117, v[102:103], off nt
	v_add_co_u32_e32 v102, vcc, s2, v0
	s_mov_b32 s2, 0x63000
	s_nop 0
	v_addc_co_u32_e32 v103, vcc, 0, v1, vcc
	global_load_dword v118, v[102:103], off nt
	v_add_co_u32_e32 v102, vcc, s2, v0
	s_mov_b32 s2, 0x62000
	s_nop 0
	v_addc_co_u32_e32 v103, vcc, 0, v1, vcc
	global_load_dword v119, v[102:103], off nt
	v_add_co_u32_e32 v102, vcc, s2, v0
	s_mov_b32 s2, 0x61000
	s_nop 0
	v_addc_co_u32_e32 v103, vcc, 0, v1, vcc
	global_load_dword v120, v[102:103], off nt
	v_add_co_u32_e32 v102, vcc, s2, v0
	s_mov_b32 s2, 0x7f000
	s_nop 0
	v_addc_co_u32_e32 v103, vcc, 0, v1, vcc
	global_load_dword v102, v[102:103], off nt
	s_nop 0
	global_load_dword v103, v[4:5], off nt
	v_add_co_u32_e32 v4, vcc, s2, v0
	s_mov_b32 s2, 0x7e000
	s_nop 0
	v_addc_co_u32_e32 v5, vcc, 0, v1, vcc
	global_load_dword v121, v[4:5], off nt
	v_add_co_u32_e32 v4, vcc, s2, v0
	s_mov_b32 s2, 0x7d000
	s_nop 0
	v_addc_co_u32_e32 v5, vcc, 0, v1, vcc
	global_load_dword v122, v[4:5], off nt
	v_add_co_u32_e32 v4, vcc, s2, v0
	s_mov_b32 s2, 0x7c000
	s_nop 0
	v_addc_co_u32_e32 v5, vcc, 0, v1, vcc
	global_load_dword v123, v[4:5], off nt
	v_add_co_u32_e32 v4, vcc, s2, v0
	s_mov_b32 s2, 0x7b000
	s_nop 0
	v_addc_co_u32_e32 v5, vcc, 0, v1, vcc
	global_load_dword v124, v[4:5], off nt
	v_add_co_u32_e32 v4, vcc, s2, v0
	s_mov_b32 s2, 0x7a000
	s_nop 0
	v_addc_co_u32_e32 v5, vcc, 0, v1, vcc
	global_load_dword v125, v[4:5], off nt
	v_add_co_u32_e32 v4, vcc, s2, v0
	s_mov_b32 s2, 0x79000
	s_nop 0
	v_addc_co_u32_e32 v5, vcc, 0, v1, vcc
	global_load_dword v126, v[4:5], off nt
	v_add_co_u32_e32 v4, vcc, s2, v0
	s_mov_b32 s2, 0x78000
	s_nop 0
	v_addc_co_u32_e32 v5, vcc, 0, v1, vcc
	global_load_dword v127, v[4:5], off nt
	v_add_co_u32_e32 v4, vcc, s2, v0
	s_mov_b32 s2, 0x77000
	s_nop 0
	v_addc_co_u32_e32 v5, vcc, 0, v1, vcc
	global_load_dword v128, v[4:5], off nt
	v_add_co_u32_e32 v4, vcc, s2, v0
	s_mov_b32 s2, 0x76000
	s_nop 0
	v_addc_co_u32_e32 v5, vcc, 0, v1, vcc
	global_load_dword v129, v[4:5], off nt
	v_add_co_u32_e32 v4, vcc, s2, v0
	s_mov_b32 s2, 0x75000
	s_nop 0
	v_addc_co_u32_e32 v5, vcc, 0, v1, vcc
	global_load_dword v130, v[4:5], off nt
	v_add_co_u32_e32 v4, vcc, s2, v0
	s_mov_b32 s2, 0x74000
	s_nop 0
	v_addc_co_u32_e32 v5, vcc, 0, v1, vcc
	global_load_dword v131, v[4:5], off nt
	v_add_co_u32_e32 v4, vcc, s2, v0
	s_mov_b32 s2, 0x73000
	s_nop 0
	v_addc_co_u32_e32 v5, vcc, 0, v1, vcc
	global_load_dword v132, v[4:5], off nt
	v_add_co_u32_e32 v4, vcc, s2, v0
	s_mov_b32 s2, 0x72000
	s_nop 0
	v_addc_co_u32_e32 v5, vcc, 0, v1, vcc
	global_load_dword v133, v[4:5], off nt
	v_add_co_u32_e32 v4, vcc, s2, v0
	s_mov_b32 s2, 0x71000
	s_nop 0
	v_addc_co_u32_e32 v5, vcc, 0, v1, vcc
	v_add_co_u32_e32 v0, vcc, s2, v0
	global_load_dword v4, v[4:5], off nt
	s_nop 0
	v_addc_co_u32_e32 v1, vcc, 0, v1, vcc
	global_load_dword v5, v[0:1], off nt
	global_load_dword v134, v[2:3], off nt
	v_mov_b32_e32 v0, s4
	s_movk_i32 s2, 0x90
	s_waitcnt vmcnt(62)
	v_mad_u32_u24 v135, v6, s2, v0
	v_mul_f32_e32 v1, 0x42800000, v26
	v_mul_f32_e32 v2, 0x42800000, v23
	v_mov_b32_e32 v0, v97
	v_cvt_pk_fp8_f32 v0, v1, v2
	v_mul_f32_e32 v3, 0x42800000, v21
	v_mul_f32_e32 v19, 0x42800000, v19
	v_mul_f32_e32 v2, 0x42800000, v18
	v_cvt_pk_fp8_f32 v0, v3, v19 op_sel:[0,0,1]
	v_mul_f32_e32 v3, 0x42800000, v17
	v_mov_b32_e32 v1, v97
	v_cvt_pk_fp8_f32 v1, v2, v3
	v_mul_f32_e32 v3, 0x42800000, v14
	v_mul_f32_e32 v13, 0x42800000, v13
	v_mov_b32_e32 v2, v97
	v_cvt_pk_fp8_f32 v2, v3, v13
	v_mul_f32_e32 v10, 0x42800000, v10
	v_mul_f32_e32 v9, 0x42800000, v9
	v_mov_b32_e32 v3, v97
	v_cvt_pk_fp8_f32 v3, v10, v9
	v_mul_f32_e32 v16, 0x42800000, v16
	v_mul_f32_e32 v15, 0x42800000, v15
	v_mul_f32_e32 v12, 0x42800000, v12
	v_mul_f32_e32 v11, 0x42800000, v11
	v_mul_f32_e32 v8, 0x42800000, v8
	v_mul_f32_e32 v7, 0x42800000, v7
	v_cvt_pk_fp8_f32 v1, v16, v15 op_sel:[0,0,1]
	v_cvt_pk_fp8_f32 v2, v12, v11 op_sel:[0,0,1]
	v_cvt_pk_fp8_f32 v3, v8, v7 op_sel:[0,0,1]
	s_waitcnt vmcnt(48)
	s_waitcnt vmcnt(32)
	s_waitcnt vmcnt(16)
	s_waitcnt vmcnt(0)
	ds_write_b128 v135, v[0:3]
	v_mul_f32_e32 v1, 0x42800000, v42
	v_mul_f32_e32 v2, 0x42800000, v41
	v_mov_b32_e32 v0, v97
	v_cvt_pk_fp8_f32 v0, v1, v2
	v_mul_f32_e32 v3, 0x42800000, v39
	v_mul_f32_e32 v7, 0x42800000, v37
	v_mul_f32_e32 v2, 0x42800000, v35
	v_cvt_pk_fp8_f32 v0, v3, v7 op_sel:[0,0,1]
	v_mul_f32_e32 v3, 0x42800000, v33
	v_mov_b32_e32 v1, v97
	v_cvt_pk_fp8_f32 v1, v2, v3
	v_mul_f32_e32 v7, 0x42800000, v32
	v_mul_f32_e32 v8, 0x42800000, v31
	v_mul_f32_e32 v3, 0x42800000, v30
	v_cvt_pk_fp8_f32 v1, v7, v8 op_sel:[0,0,1]
	v_mul_f32_e32 v7, 0x42800000, v29
	v_mov_b32_e32 v2, v97
	v_cvt_pk_fp8_f32 v2, v3, v7
	v_mul_f32_e32 v8, 0x42800000, v28
	v_mul_f32_e32 v9, 0x42800000, v27
	v_mul_f32_e32 v7, 0x42800000, v25
	v_cvt_pk_fp8_f32 v2, v8, v9 op_sel:[0,0,1]
	v_mul_f32_e32 v8, 0x42800000, v24
	v_mov_b32_e32 v3, v97
	v_cvt_pk_fp8_f32 v3, v7, v8
	v_mul_f32_e32 v9, 0x42800000, v22
	v_mul_f32_e32 v10, 0x42800000, v20
	v_mul_f32_e32 v7, 0x42800000, v53
	v_cvt_pk_fp8_f32 v3, v9, v10 op_sel:[0,0,1]
	v_mul_f32_e32 v8, 0x42800000, v47
	v_mul_f32_e32 v9, 0x42800000, v43
	v_mul_f32_e32 v10, 0x42800000, v34
	ds_write_b128 v135, v[0:3] offset:16
	v_mul_f32_e32 v1, 0x42800000, v58
	v_mul_f32_e32 v2, 0x42800000, v57
	v_mov_b32_e32 v0, v97
	v_cvt_pk_fp8_f32 v0, v1, v2
	v_mul_f32_e32 v3, 0x42800000, v55
	v_mul_f32_e32 v2, 0x42800000, v51
	v_mov_b32_e32 v1, v97
	v_cvt_pk_fp8_f32 v0, v3, v7 op_sel:[0,0,1]
	v_mul_f32_e32 v3, 0x42800000, v49
	v_cvt_pk_fp8_f32 v1, v2, v3
	v_mul_f32_e32 v7, 0x42800000, v48
	v_mul_f32_e32 v3, 0x42800000, v46
	v_mov_b32_e32 v2, v97
	v_cvt_pk_fp8_f32 v1, v7, v8 op_sel:[0,0,1]
	v_mul_f32_e32 v7, 0x42800000, v45
	v_cvt_pk_fp8_f32 v2, v3, v7
	v_mul_f32_e32 v8, 0x42800000, v44
	v_mul_f32_e32 v7, 0x42800000, v40
	v_mov_b32_e32 v3, v97
	v_cvt_pk_fp8_f32 v2, v8, v9 op_sel:[0,0,1]
	v_mul_f32_e32 v8, 0x42800000, v38
	v_cvt_pk_fp8_f32 v3, v7, v8
	v_mul_f32_e32 v9, 0x42800000, v36
	v_mul_f32_e32 v7, 0x42800000, v69
	v_mul_f32_e32 v8, 0x42800000, v63
	v_cvt_pk_fp8_f32 v3, v9, v10 op_sel:[0,0,1]
	v_mul_f32_e32 v9, 0x42800000, v59
	v_mul_f32_e32 v10, 0x42800000, v50
	s_add_u32 s2, s12, s14
	ds_write_b128 v135, v[0:3] offset:32
	v_mul_f32_e32 v1, 0x42800000, v74
	v_mul_f32_e32 v2, 0x42800000, v73
	v_mov_b32_e32 v0, v97
	v_cvt_pk_fp8_f32 v0, v1, v2
	v_mul_f32_e32 v3, 0x42800000, v71
	v_mul_f32_e32 v2, 0x42800000, v67
	v_mov_b32_e32 v1, v97
	v_cvt_pk_fp8_f32 v0, v3, v7 op_sel:[0,0,1]
	v_mul_f32_e32 v3, 0x42800000, v65
	v_cvt_pk_fp8_f32 v1, v2, v3
	v_mul_f32_e32 v7, 0x42800000, v64
	v_mul_f32_e32 v3, 0x42800000, v62
	v_mov_b32_e32 v2, v97
	v_cvt_pk_fp8_f32 v1, v7, v8 op_sel:[0,0,1]
	v_mul_f32_e32 v7, 0x42800000, v61
	v_cvt_pk_fp8_f32 v2, v3, v7
	v_mul_f32_e32 v8, 0x42800000, v60
	v_mul_f32_e32 v7, 0x42800000, v56
	v_mov_b32_e32 v3, v97
	v_cvt_pk_fp8_f32 v2, v8, v9 op_sel:[0,0,1]
	v_mul_f32_e32 v8, 0x42800000, v54
	v_cvt_pk_fp8_f32 v3, v7, v8
	v_mul_f32_e32 v9, 0x42800000, v52
	v_mul_f32_e32 v7, 0x42800000, v85
	v_mul_f32_e32 v8, 0x42800000, v79
	v_cvt_pk_fp8_f32 v3, v9, v10 op_sel:[0,0,1]
	v_mul_f32_e32 v9, 0x42800000, v75
	v_mul_f32_e32 v10, 0x42800000, v66
	s_addc_u32 s3, s13, 0
	ds_write_b128 v135, v[0:3] offset:48
	v_mul_f32_e32 v1, 0x42800000, v90
	v_mul_f32_e32 v2, 0x42800000, v89
	v_mov_b32_e32 v0, v97
	v_cvt_pk_fp8_f32 v0, v1, v2
	v_mul_f32_e32 v3, 0x42800000, v87
	v_mul_f32_e32 v2, 0x42800000, v83
	v_mov_b32_e32 v1, v97
	v_cvt_pk_fp8_f32 v0, v3, v7 op_sel:[0,0,1]
	v_mul_f32_e32 v3, 0x42800000, v81
	v_cvt_pk_fp8_f32 v1, v2, v3
	v_mul_f32_e32 v7, 0x42800000, v80
	v_mul_f32_e32 v3, 0x42800000, v78
	v_mov_b32_e32 v2, v97
	v_cvt_pk_fp8_f32 v1, v7, v8 op_sel:[0,0,1]
	v_mul_f32_e32 v7, 0x42800000, v77
	v_cvt_pk_fp8_f32 v2, v3, v7
	v_mul_f32_e32 v8, 0x42800000, v76
	v_mul_f32_e32 v7, 0x42800000, v72
	v_mov_b32_e32 v3, v97
	v_cvt_pk_fp8_f32 v2, v8, v9 op_sel:[0,0,1]
	v_mul_f32_e32 v8, 0x42800000, v70
	v_cvt_pk_fp8_f32 v3, v7, v8
	v_mul_f32_e32 v9, 0x42800000, v68
	v_mul_f32_e32 v7, 0x42800000, v104
	v_mul_f32_e32 v8, 0x42800000, v95
	v_cvt_pk_fp8_f32 v3, v9, v10 op_sel:[0,0,1]
	v_mul_f32_e32 v9, 0x42800000, v91
	v_mul_f32_e32 v10, 0x42800000, v82
	ds_write_b128 v135, v[0:3] offset:64
	v_mul_f32_e32 v1, 0x42800000, v107
	v_mul_f32_e32 v2, 0x42800000, v106
	v_mov_b32_e32 v0, v97
	v_cvt_pk_fp8_f32 v0, v1, v2
	v_mul_f32_e32 v3, 0x42800000, v105
	v_mul_f32_e32 v2, 0x42800000, v101
	v_mov_b32_e32 v1, v97
	v_cvt_pk_fp8_f32 v0, v3, v7 op_sel:[0,0,1]
	v_mul_f32_e32 v3, 0x42800000, v99
	v_cvt_pk_fp8_f32 v1, v2, v3
	v_mul_f32_e32 v7, 0x42800000, v98
	v_mul_f32_e32 v3, 0x42800000, v94
	v_mov_b32_e32 v2, v97
	v_cvt_pk_fp8_f32 v1, v7, v8 op_sel:[0,0,1]
	v_mul_f32_e32 v7, 0x42800000, v93
	v_cvt_pk_fp8_f32 v2, v3, v7
	v_mul_f32_e32 v8, 0x42800000, v92
	v_mul_f32_e32 v7, 0x42800000, v88
	v_mov_b32_e32 v3, v97
	v_cvt_pk_fp8_f32 v2, v8, v9 op_sel:[0,0,1]
	v_mul_f32_e32 v8, 0x42800000, v86
	v_cvt_pk_fp8_f32 v3, v7, v8
	v_mul_f32_e32 v9, 0x42800000, v84
	v_mul_f32_e32 v7, 0x42800000, v119
	v_mul_f32_e32 v8, 0x42800000, v115
	v_cvt_pk_fp8_f32 v3, v9, v10 op_sel:[0,0,1]
	v_mul_f32_e32 v9, 0x42800000, v111
	v_mul_f32_e32 v10, 0x42800000, v100
	ds_write_b128 v135, v[0:3] offset:80
	v_mul_f32_e32 v1, 0x42800000, v103
	v_mul_f32_e32 v2, 0x42800000, v102
	v_mov_b32_e32 v0, v97
	v_cvt_pk_fp8_f32 v0, v1, v2
	v_mul_f32_e32 v3, 0x42800000, v120
	v_mul_f32_e32 v2, 0x42800000, v118
	v_mov_b32_e32 v1, v97
	v_cvt_pk_fp8_f32 v0, v3, v7 op_sel:[0,0,1]
	v_mul_f32_e32 v3, 0x42800000, v117
	v_cvt_pk_fp8_f32 v1, v2, v3
	v_mul_f32_e32 v7, 0x42800000, v116
	v_mul_f32_e32 v3, 0x42800000, v114
	v_mov_b32_e32 v2, v97
	v_cvt_pk_fp8_f32 v1, v7, v8 op_sel:[0,0,1]
	v_mul_f32_e32 v7, 0x42800000, v113
	v_cvt_pk_fp8_f32 v2, v3, v7
	v_mul_f32_e32 v8, 0x42800000, v112
	v_mul_f32_e32 v7, 0x42800000, v110
	v_mov_b32_e32 v3, v97
	v_cvt_pk_fp8_f32 v2, v8, v9 op_sel:[0,0,1]
	v_mul_f32_e32 v8, 0x42800000, v109
	v_cvt_pk_fp8_f32 v3, v7, v8
	v_mul_f32_e32 v9, 0x42800000, v108
	v_mul_f32_e32 v7, 0x42800000, v125
	v_mul_f32_e32 v8, 0x42800000, v121
	v_cvt_pk_fp8_f32 v3, v9, v10 op_sel:[0,0,1]
	v_mov_b32_e32 v9, v97
	ds_write_b128 v135, v[0:3] offset:96
	v_mul_f32_e32 v1, 0x42800000, v134
	v_mul_f32_e32 v2, 0x42800000, v5
	v_mov_b32_e32 v0, v97
	v_cvt_pk_fp8_f32 v0, v1, v2
	v_mul_f32_e32 v3, 0x42800000, v4
	v_mul_f32_e32 v4, 0x42800000, v133
	v_mul_f32_e32 v2, 0x42800000, v132
	v_cvt_pk_fp8_f32 v0, v3, v4 op_sel:[0,0,1]
	v_mul_f32_e32 v3, 0x42800000, v131
	v_mov_b32_e32 v1, v97
	v_cvt_pk_fp8_f32 v1, v2, v3
	v_mul_f32_e32 v4, 0x42800000, v130
	v_mul_f32_e32 v5, 0x42800000, v129
	v_mul_f32_e32 v3, 0x42800000, v128
	v_cvt_pk_fp8_f32 v1, v4, v5 op_sel:[0,0,1]
	v_mul_f32_e32 v4, 0x42800000, v127
	v_mov_b32_e32 v2, v97
	v_cvt_pk_fp8_f32 v2, v3, v4
	v_mul_f32_e32 v5, 0x42800000, v126
	v_mul_f32_e32 v4, 0x42800000, v124
	v_mov_b32_e32 v3, v97
	v_cvt_pk_fp8_f32 v2, v5, v7 op_sel:[0,0,1]
	v_mul_f32_e32 v5, 0x42800000, v123
	v_cvt_pk_fp8_f32 v3, v4, v5
	v_mul_f32_e32 v7, 0x42800000, v122
	v_cvt_pk_fp8_f32 v3, v7, v8 op_sel:[0,0,1]
	v_lshrrev_b32_e32 v8, 3, v6
	ds_write_b128 v135, v[0:3] offset:112
	v_lshlrev_b32_e32 v0, 4, v6
	v_and_b32_e32 v0, 0x70, v0
	v_mov_b32_e32 v1, v97
	v_lshl_add_u64 v[4:5], s[2:3], 0, v[0:1]
	v_mul_u32_u24_e32 v1, 0x90, v8
	s_waitcnt lgkmcnt(0)
	v_add3_u32 v7, s4, v0, v1
	ds_read_b128 v[0:3], v7
	v_or_b32_e32 v8, s7, v8
	v_lshlrev_b32_e32 v8, 10, v8
	v_lshl_add_u64 v[10:11], v[4:5], 0, v[8:9]
	s_mov_b64 s[2:3], 0
	s_waitcnt lgkmcnt(0)
	global_store_dwordx4 v[10:11], v[0:3], off
	ds_read_b128 v[0:3], v7 offset:1152
	v_or_b32_e32 v10, 0x2000, v8
	v_mov_b32_e32 v11, v97
	v_lshl_add_u64 v[10:11], v[4:5], 0, v[10:11]
	s_waitcnt lgkmcnt(0)
	global_store_dwordx4 v[10:11], v[0:3], off
	ds_read_b128 v[0:3], v7 offset:2304
	v_or_b32_e32 v10, 0x4000, v8
	v_mov_b32_e32 v11, v97
	v_lshl_add_u64 v[10:11], v[4:5], 0, v[10:11]
	s_waitcnt lgkmcnt(0)
	global_store_dwordx4 v[10:11], v[0:3], off
	ds_read_b128 v[0:3], v7 offset:3456
	v_or_b32_e32 v10, 0x6000, v8
	v_mov_b32_e32 v11, v97
	v_lshl_add_u64 v[10:11], v[4:5], 0, v[10:11]
	s_waitcnt lgkmcnt(0)
	global_store_dwordx4 v[10:11], v[0:3], off
	ds_read_b128 v[0:3], v7 offset:4608
	v_or_b32_e32 v10, 0x8000, v8
	v_mov_b32_e32 v11, v97
	v_lshl_add_u64 v[10:11], v[4:5], 0, v[10:11]
	s_waitcnt lgkmcnt(0)
	global_store_dwordx4 v[10:11], v[0:3], off
	ds_read_b128 v[0:3], v7 offset:5760
	v_or_b32_e32 v10, 0xa000, v8
	v_mov_b32_e32 v11, v97
	v_lshl_add_u64 v[10:11], v[4:5], 0, v[10:11]
	s_waitcnt lgkmcnt(0)
	global_store_dwordx4 v[10:11], v[0:3], off
	ds_read_b128 v[0:3], v7 offset:6912
	v_or_b32_e32 v10, 0xc000, v8
	v_mov_b32_e32 v11, v97
	v_lshl_add_u64 v[10:11], v[4:5], 0, v[10:11]
	v_or_b32_e32 v8, 0xe000, v8
	s_waitcnt lgkmcnt(0)
	global_store_dwordx4 v[10:11], v[0:3], off
	ds_read_b128 v[0:3], v7 offset:8064
	v_lshl_add_u64 v[4:5], v[4:5], 0, v[8:9]
	s_waitcnt lgkmcnt(0)
	global_store_dwordx4 v[4:5], v[0:3], off
	s_waitcnt lgkmcnt(0)
